# non-temporal (nt) hint on the read-once streams: prologue weight tile loads and layer-0 rowpass input rows
# speedup vs baseline: 1.0022x; 1.0022x over previous
.LBB0_14:
	s_mul_hi_i32 s2, s30, 0x9c09c09d
	s_add_i32 s2, s2, s30
	s_lshr_b32 s16, s2, 31
	s_ashr_i32 s2, s2, 14
	s_add_i32 s16, s2, s16
	s_mul_i32 s2, s16, 0xffff9700
	s_add_i32 s20, s30, s2
	s_cmpk_gt_i32 s20, 0x6ff
	s_mov_b64 s[18:19], -1
	s_cbranch_scc0 .LBB0_28
	s_cmpk_gt_u32 s20, 0x7ff
	s_cbranch_scc0 .LBB0_25
	s_cmpk_gt_u32 s20, 0x8ff
	s_cbranch_scc0 .LBB0_22
	s_cmpk_gt_u32 s20, 0x48ff
	s_cbranch_scc0 .LBB0_19
	s_lshl_b32 s19, s30, 1
	s_add_i32 s2, s20, 0xffffb700
	s_and_b32 s18, s45, 0x3c0
	s_and_b32 s19, s19, 32
	s_lshr_b32 s2, s2, 8
	s_or_b32 s21, s19, s18
	s_lshl_b32 s18, s16, 5
	s_lshl_b32 s17, s30, 2
	s_add_i32 s18, s2, s18
	s_and_b32 s17, s17, 0x380
	s_ashr_i32 s19, s18, 31
	s_lshl_b64 s[22:23], s[18:19], 22
	s_lshl_b32 s2, s17, 12
	s_waitcnt lgkmcnt(0)
	s_add_u32 s22, s6, s22
	s_addc_u32 s23, s7, s23
	s_add_u32 s2, s22, s2
	s_addc_u32 s23, s23, 0
	s_lshl_b32 s22, s21, 2
	s_add_u32 s22, s2, s22
	s_addc_u32 s23, s23, 0
	v_lshl_add_u64 v[2:3], s[22:23], 0, v[106:107]
	v_lshlrev_b32_e32 v66, 2, v184
	v_lshl_add_u64 v[62:63], v[2:3], 0, v[66:67]
	v_add_co_u32_e32 v6, vcc, s48, v62
	s_lshl_b64 s[18:19], s[18:19], 20
	s_nop 0
	v_addc_co_u32_e32 v7, vcc, 0, v63, vcc
	v_add_co_u32_e32 v10, vcc, s49, v62
	global_load_dwordx4 v[2:5], v[62:63], off nt
	s_nop 0
	global_load_dwordx4 v[6:9], v[6:7], off nt
	v_addc_co_u32_e32 v11, vcc, 0, v63, vcc
	v_add_co_u32_e32 v14, vcc, s50, v62
	s_add_u32 s2, s31, s18
	s_nop 0
	v_addc_co_u32_e32 v15, vcc, 0, v63, vcc
	global_load_dwordx4 v[10:13], v[10:11], off nt
	s_nop 0
	global_load_dwordx4 v[14:17], v[14:15], off nt
	v_add_co_u32_e32 v18, vcc, s51, v62
	s_addc_u32 s18, s33, s19
	s_nop 0
	v_addc_co_u32_e32 v19, vcc, 0, v63, vcc
	v_add_co_u32_e32 v22, vcc, s52, v62
	s_lshl_b32 s19, s21, 10
	s_nop 0
	v_addc_co_u32_e32 v23, vcc, 0, v63, vcc
	global_load_dwordx4 v[18:21], v[18:19], off nt
	s_nop 0
	global_load_dwordx4 v[22:25], v[22:23], off nt
	v_add_co_u32_e32 v26, vcc, s53, v62
	s_add_u32 s2, s2, s19
	s_nop 0
	v_addc_co_u32_e32 v27, vcc, 0, v63, vcc
	v_add_co_u32_e32 v30, vcc, s54, v62
	s_addc_u32 s19, s18, 0
	s_nop 0
	v_addc_co_u32_e32 v31, vcc, 0, v63, vcc
	global_load_dwordx4 v[26:29], v[26:27], off nt
	s_nop 0
	global_load_dwordx4 v[30:33], v[30:31], off nt
	v_add_co_u32_e32 v34, vcc, s55, v62
	s_add_u32 s18, s2, s17
	s_nop 0
	v_addc_co_u32_e32 v35, vcc, 0, v63, vcc
	v_add_co_u32_e32 v38, vcc, s56, v62
	s_addc_u32 s19, s19, 0
	s_nop 0
	v_addc_co_u32_e32 v39, vcc, 0, v63, vcc
	global_load_dwordx4 v[34:37], v[34:35], off nt
	s_nop 0
	global_load_dwordx4 v[38:41], v[38:39], off nt
	v_add_co_u32_e32 v42, vcc, s57, v62
	s_nop 1
	v_addc_co_u32_e32 v43, vcc, 0, v63, vcc
	v_add_co_u32_e32 v46, vcc, s58, v62
	s_nop 1
	v_addc_co_u32_e32 v47, vcc, 0, v63, vcc
	global_load_dwordx4 v[42:45], v[42:43], off nt
	s_nop 0
	global_load_dwordx4 v[46:49], v[46:47], off nt
	v_add_co_u32_e32 v50, vcc, s59, v62
	s_nop 1
	v_addc_co_u32_e32 v51, vcc, 0, v63, vcc
	global_load_dwordx4 v[50:53], v[50:51], off nt
	v_add_co_u32_e32 v54, vcc, s60, v62
	s_nop 1
	v_addc_co_u32_e32 v55, vcc, 0, v63, vcc
	global_load_dwordx4 v[54:57], v[54:55], off nt
	v_add_co_u32_e32 v58, vcc, s61, v62
	s_nop 1
	v_addc_co_u32_e32 v59, vcc, 0, v63, vcc
	global_load_dwordx4 v[58:61], v[58:59], off nt
	v_add_co_u32_e32 v62, vcc, s62, v62
	s_nop 1
	v_addc_co_u32_e32 v63, vcc, 0, v63, vcc
	global_load_dwordx4 v[62:65], v[62:63], off nt
	s_waitcnt vmcnt(15)
	ds_write2_b32 v71, v2, v3 offset1:1
	ds_write2_b32 v71, v4, v5 offset0:2 offset1:3
	v_add_u32_e32 v2, 0x420, v71
	s_waitcnt vmcnt(14)
	ds_write2_b32 v2, v6, v7 offset1:1
	v_add_u32_e32 v2, 0x428, v71
	ds_write2_b32 v2, v8, v9 offset1:1
	v_add_u32_e32 v2, 0x840, v71
	s_waitcnt vmcnt(13)
	ds_write2_b32 v2, v10, v11 offset1:1
	v_add_u32_e32 v2, 0x848, v71
	ds_write2_b32 v2, v12, v13 offset1:1
	v_add_u32_e32 v2, 0xc60, v71
	s_waitcnt vmcnt(12)
	ds_write2_b32 v2, v14, v15 offset1:1
	v_add_u32_e32 v2, 0xc68, v71
	ds_write2_b32 v2, v16, v17 offset1:1
	v_add_u32_e32 v2, 0x1080, v71
	s_waitcnt vmcnt(11)
	ds_write2_b32 v2, v18, v19 offset1:1
	v_add_u32_e32 v2, 0x1088, v71
	ds_write2_b32 v2, v20, v21 offset1:1
	v_add_u32_e32 v2, 0x14a0, v71
	s_waitcnt vmcnt(10)
	ds_write2_b32 v2, v22, v23 offset1:1
	v_add_u32_e32 v2, 0x14a8, v71
	ds_write2_b32 v2, v24, v25 offset1:1
	v_add_u32_e32 v2, 0x18c0, v71
	s_waitcnt vmcnt(9)
	ds_write2_b32 v2, v26, v27 offset1:1
	v_add_u32_e32 v2, 0x18c8, v71
	ds_write2_b32 v2, v28, v29 offset1:1
	v_add_u32_e32 v2, 0x1ce0, v71
	s_waitcnt vmcnt(8)
	ds_write2_b32 v2, v30, v31 offset1:1
	v_add_u32_e32 v2, 0x1ce8, v71
	ds_write2_b32 v2, v32, v33 offset1:1
	v_add_u32_e32 v2, 0x2100, v71
	s_waitcnt vmcnt(7)
	ds_write2_b32 v2, v34, v35 offset1:1
	v_add_u32_e32 v2, 0x2108, v71
	ds_write2_b32 v2, v36, v37 offset1:1
	v_add_u32_e32 v2, 0x2520, v71
	s_waitcnt vmcnt(6)
	ds_write2_b32 v2, v38, v39 offset1:1
	v_add_u32_e32 v2, 0x2528, v71
	ds_write2_b32 v2, v40, v41 offset1:1
	v_add_u32_e32 v2, 0x2940, v71
	v_lshl_add_u64 v[38:39], s[18:19], 0, v[68:69]
	v_lshl_add_u64 v[40:41], v[38:39], 0, v[108:109]
	s_mov_b64 s[18:19], 0
	s_waitcnt vmcnt(5)
	ds_write2_b32 v2, v42, v43 offset1:1
	v_add_u32_e32 v2, 0x2948, v71
	ds_write2_b32 v2, v44, v45 offset1:1
	v_add_u32_e32 v2, 0x2d60, v71
	s_waitcnt vmcnt(4)
	ds_write2_b32 v2, v46, v47 offset1:1
	v_add_u32_e32 v2, 0x2d68, v71
	ds_write2_b32 v2, v48, v49 offset1:1
	v_add_u32_e32 v2, 0x3180, v71
	s_waitcnt vmcnt(3)
	ds_write2_b32 v2, v50, v51 offset1:1
	v_add_u32_e32 v2, 0x3188, v71
	ds_write2_b32 v2, v52, v53 offset1:1
	v_add_u32_e32 v2, 0x35a0, v71
	v_add_u32_e32 v42, 0x400, v119
	s_waitcnt vmcnt(2)
	ds_write2_b32 v2, v54, v55 offset1:1
	v_add_u32_e32 v2, 0x35a8, v71
	ds_write2_b32 v2, v56, v57 offset1:1
	v_add_u32_e32 v2, 0x39c0, v71
	s_waitcnt vmcnt(1)
	ds_write2_b32 v2, v58, v59 offset1:1
	v_add_u32_e32 v2, 0x39c8, v71
	ds_write2_b32 v2, v60, v61 offset1:1
	v_add_u32_e32 v2, 0x3de0, v71
	s_waitcnt vmcnt(0)
	ds_write2_b32 v2, v62, v63 offset1:1
	v_add_u32_e32 v2, 0x3de8, v71
	ds_write2_b32 v2, v64, v65 offset1:1
	s_waitcnt lgkmcnt(0)
	ds_read2_b32 v[6:7], v119 offset0:66 offset1:74
	ds_read2_b32 v[8:9], v119 offset0:99 offset1:107
	ds_read2_b32 v[10:11], v119 offset1:8
	ds_read2_b32 v[12:13], v119 offset0:33 offset1:41
	v_mov_b32_e32 v2, v67
	s_waitcnt lgkmcnt(3)
	v_mul_f32_e32 v3, 0x42000000, v6
	ds_read2_b32 v[14:15], v119 offset0:198 offset1:206
	ds_read2_b32 v[16:17], v119 offset0:231 offset1:239
	ds_read2_b32 v[18:19], v119 offset0:132 offset1:140
	ds_read2_b32 v[20:21], v119 offset0:165 offset1:173
	s_waitcnt lgkmcnt(5)
	v_mul_f32_e32 v5, 0x42000000, v10
	s_waitcnt lgkmcnt(4)
	v_mul_f32_e32 v6, 0x42000000, v12
	v_cvt_pk_fp8_f32 v2, v5, v6
	v_mul_f32_e32 v4, 0x42000000, v8
	s_waitcnt lgkmcnt(1)
	v_mul_f32_e32 v6, 0x42000000, v18
	s_waitcnt lgkmcnt(0)
	v_mul_f32_e32 v8, 0x42000000, v20
	v_cvt_pk_fp8_f32 v2, v3, v4 op_sel:[0,0,1]
	v_mov_b32_e32 v3, v67
	ds_read2_b32 v[22:23], v42 offset0:74 offset1:82
	ds_read2_b32 v[24:25], v42 offset0:107 offset1:115
	ds_read2_b32 v[26:27], v42 offset0:8 offset1:16
	ds_read2_b32 v[28:29], v42 offset0:41 offset1:49
	v_cvt_pk_fp8_f32 v3, v6, v8
	ds_read2_b32 v[30:31], v42 offset0:140 offset1:148
	ds_read2_b32 v[32:33], v42 offset0:173 offset1:181
	v_mul_f32_e32 v4, 0x42000000, v14
	v_mul_f32_e32 v5, 0x42000000, v16
	v_cvt_pk_fp8_f32 v3, v4, v5 op_sel:[0,0,1]
	s_waitcnt lgkmcnt(3)
	v_mul_f32_e32 v5, 0x42000000, v26
	s_waitcnt lgkmcnt(2)
	v_mul_f32_e32 v10, 0x42000000, v28
	v_mov_b32_e32 v4, v67
	ds_read2_b32 v[34:35], v42 offset0:206 offset1:214
	ds_read2_b32 v[36:37], v42 offset0:239 offset1:247
	v_cvt_pk_fp8_f32 v4, v5, v10
	s_waitcnt lgkmcnt(3)
	v_mul_f32_e32 v10, 0x42000000, v30
	s_waitcnt lgkmcnt(2)
	v_mul_f32_e32 v12, 0x42000000, v32
	v_mov_b32_e32 v5, v67
	v_cvt_pk_fp8_f32 v5, v10, v12
	v_mul_f32_e32 v6, 0x42000000, v22
	v_mul_f32_e32 v8, 0x42000000, v24
	v_cvt_pk_fp8_f32 v4, v6, v8 op_sel:[0,0,1]
	s_waitcnt lgkmcnt(1)
	v_mul_f32_e32 v6, 0x42000000, v34
	s_waitcnt lgkmcnt(0)
	v_mul_f32_e32 v8, 0x42000000, v36
	v_cvt_pk_fp8_f32 v5, v6, v8 op_sel:[0,0,1]
	v_mul_f32_e32 v6, 0x42000000, v13
	v_mul_f32_e32 v8, 0x42000000, v29
	global_store_dwordx4 v[40:41], v[2:5], off
	s_nop 1
	v_mul_f32_e32 v3, 0x42000000, v11
	v_mov_b32_e32 v2, v67
	v_mul_f32_e32 v4, 0x42000000, v7
	v_cvt_pk_fp8_f32 v2, v3, v6
	v_mul_f32_e32 v6, 0x42000000, v19
	v_mul_f32_e32 v7, 0x42000000, v21
	v_mov_b32_e32 v3, v67
	v_cvt_pk_fp8_f32 v3, v6, v7
	v_mul_f32_e32 v5, 0x42000000, v9
	v_cvt_pk_fp8_f32 v2, v4, v5 op_sel:[0,0,1]
	v_mul_f32_e32 v4, 0x42000000, v15
	v_mul_f32_e32 v5, 0x42000000, v17
	v_cvt_pk_fp8_f32 v3, v4, v5 op_sel:[0,0,1]
	v_mul_f32_e32 v5, 0x42000000, v27
	v_mov_b32_e32 v4, v67
	v_cvt_pk_fp8_f32 v4, v5, v8
	v_mul_f32_e32 v8, 0x42000000, v31
	v_mul_f32_e32 v9, 0x42000000, v33
	v_mov_b32_e32 v5, v67
	v_cvt_pk_fp8_f32 v5, v8, v9
	v_mul_f32_e32 v6, 0x42000000, v23
	v_mul_f32_e32 v7, 0x42000000, v25
	v_cvt_pk_fp8_f32 v4, v6, v7 op_sel:[0,0,1]
	v_mul_f32_e32 v6, 0x42000000, v35
	v_mul_f32_e32 v7, 0x42000000, v37
	ds_read2_b32 v[8:9], v119 offset0:82 offset1:90
	ds_read2_b32 v[10:11], v119 offset0:115 offset1:123
	ds_read2_b32 v[12:13], v119 offset0:16 offset1:24
	ds_read2_b32 v[14:15], v119 offset0:49 offset1:57
	v_cvt_pk_fp8_f32 v5, v6, v7 op_sel:[0,0,1]
	v_lshl_add_u64 v[6:7], v[38:39], 0, v[72:73]
	global_store_dwordx4 v[6:7], v[2:5], off
	s_waitcnt lgkmcnt(1)
	s_nop 0
	v_mul_f32_e32 v5, 0x42000000, v12
	s_waitcnt lgkmcnt(0)
	v_mul_f32_e32 v6, 0x42000000, v14
	v_mov_b32_e32 v2, v67
	v_cvt_pk_fp8_f32 v2, v5, v6
	ds_read2_b32 v[16:17], v119 offset0:214 offset1:222
	ds_read2_b32 v[18:19], v119 offset0:247 offset1:255
	ds_read2_b32 v[6:7], v119 offset0:148 offset1:156
	ds_read2_b32 v[20:21], v119 offset0:181 offset1:189
	v_mul_f32_e32 v3, 0x42000000, v8
	v_mul_f32_e32 v4, 0x42000000, v10
	v_cvt_pk_fp8_f32 v2, v3, v4 op_sel:[0,0,1]
	s_waitcnt lgkmcnt(1)
	v_mul_f32_e32 v6, 0x42000000, v6
	s_waitcnt lgkmcnt(0)
	v_mul_f32_e32 v8, 0x42000000, v20
	v_mov_b32_e32 v3, v67
	ds_read2_b32 v[22:23], v42 offset0:90 offset1:98
	ds_read2_b32 v[24:25], v42 offset0:123 offset1:131
	ds_read2_b32 v[26:27], v42 offset0:24 offset1:32
	ds_read2_b32 v[28:29], v42 offset0:57 offset1:65
	v_cvt_pk_fp8_f32 v3, v6, v8
	v_mul_f32_e32 v4, 0x42000000, v16
	v_mul_f32_e32 v5, 0x42000000, v18
	ds_read2_b32 v[30:31], v42 offset0:156 offset1:164
	ds_read2_b32 v[32:33], v42 offset0:189 offset1:197
	ds_read2_b32 v[34:35], v42 offset0:222 offset1:230
	v_cvt_pk_fp8_f32 v3, v4, v5 op_sel:[0,0,1]
	s_waitcnt lgkmcnt(4)
	v_mul_f32_e32 v5, 0x42000000, v26
	s_waitcnt lgkmcnt(3)
	v_mul_f32_e32 v10, 0x42000000, v28
	v_mov_b32_e32 v4, v67
	v_cvt_pk_fp8_f32 v4, v5, v10
	v_add_u32_e32 v5, 0x600, v119
	ds_read2_b32 v[36:37], v5 offset0:127 offset1:135
	s_waitcnt lgkmcnt(3)
	v_mul_f32_e32 v10, 0x42000000, v30
	s_waitcnt lgkmcnt(2)
	v_mul_f32_e32 v12, 0x42000000, v32
	v_mov_b32_e32 v5, v67
	v_cvt_pk_fp8_f32 v5, v10, v12
	v_mul_f32_e32 v6, 0x42000000, v22
	v_mul_f32_e32 v8, 0x42000000, v24
	v_cvt_pk_fp8_f32 v4, v6, v8 op_sel:[0,0,1]
	s_waitcnt lgkmcnt(1)
	v_mul_f32_e32 v6, 0x42000000, v34
	s_waitcnt lgkmcnt(0)
	v_mul_f32_e32 v8, 0x42000000, v36
	v_cvt_pk_fp8_f32 v5, v6, v8 op_sel:[0,0,1]
	v_mul_f32_e32 v8, 0x42000000, v9
	v_mul_f32_e32 v9, 0x42000000, v11
	v_mul_f32_e32 v10, 0x42000000, v13
	v_mul_f32_e32 v11, 0x42000000, v15
	v_mov_b32_e32 v6, v67
	v_cvt_pk_fp8_f32 v6, v10, v11
	v_mul_f32_e32 v10, 0x42000000, v7
	v_mul_f32_e32 v11, 0x42000000, v21
	v_mov_b32_e32 v7, v67
	v_cvt_pk_fp8_f32 v7, v10, v11
	v_cvt_pk_fp8_f32 v6, v8, v9 op_sel:[0,0,1]
	v_mul_f32_e32 v8, 0x42000000, v17
	v_mul_f32_e32 v9, 0x42000000, v19
	v_cvt_pk_fp8_f32 v7, v8, v9 op_sel:[0,0,1]
	v_mul_f32_e32 v9, 0x42000000, v27
	v_mul_f32_e32 v12, 0x42000000, v29
	v_mov_b32_e32 v8, v67
	v_cvt_pk_fp8_f32 v8, v9, v12
	v_mul_f32_e32 v12, 0x42000000, v31
	v_mul_f32_e32 v13, 0x42000000, v33
	v_mov_b32_e32 v9, v67
	v_cvt_pk_fp8_f32 v9, v12, v13
	v_mul_f32_e32 v10, 0x42000000, v23
	v_mul_f32_e32 v11, 0x42000000, v25
	v_cvt_pk_fp8_f32 v8, v10, v11 op_sel:[0,0,1]
	v_mul_f32_e32 v10, 0x42000000, v35
	v_mul_f32_e32 v11, 0x42000000, v37
	v_cvt_pk_fp8_f32 v9, v10, v11 op_sel:[0,0,1]
	v_lshl_add_u64 v[10:11], v[38:39], 0, v[78:79]
	global_store_dwordx4 v[10:11], v[2:5], off
	s_nop 1
	v_lshl_add_u64 v[2:3], v[38:39], 0, v[84:85]
	global_store_dwordx4 v[2:3], v[6:9], off
	s_waitcnt lgkmcnt(0)
.LBB0_19:
	s_andn2_b64 vcc, exec, s[18:19]
	s_cbranch_vccnz .LBB0_21
	s_and_b32 s18, s45, 0x7c0
	s_and_b32 s19, s30, 32
	s_add_i32 s2, s20, 0xfffff700
	s_or_b32 s21, s18, s19
	s_lshr_b32 s19, s45, 1
	s_lshr_b32 s17, s2, 9
	s_lshl_b32 s2, s16, 9
	s_and_b32 s18, s21, 0xe0
	s_and_b32 s19, s19, 0x380
	s_sub_i32 s2, s47, s2
	s_or_b32 s22, s18, s19
	s_add_i32 s19, s19, s18
	s_and_b32 s2, s2, 0x380
	s_addk_i32 s19, 0x380
	s_cmpk_lt_u32 s18, 0x80
	s_cselect_b32 s24, s22, s19
	s_lshl_b32 s18, s16, 5
	s_add_i32 s18, s17, s18
	s_ashr_i32 s19, s18, 31
	s_lshl_b64 s[22:23], s[18:19], 23
	s_waitcnt lgkmcnt(0)
	s_add_u32 s17, s12, s22
	s_addc_u32 s22, s13, s23
	s_lshl_b32 s23, s2, 13
	s_add_u32 s17, s17, s23
	s_addc_u32 s23, s22, 0
	s_lshl_b32 s22, s24, 2
	s_add_u32 s22, s17, s22
	s_addc_u32 s23, s23, 0
	v_lshl_add_u64 v[2:3], s[22:23], 0, v[110:111]
	v_lshlrev_b32_e32 v66, 2, v184
	v_lshl_add_u64 v[62:63], v[2:3], 0, v[66:67]
	v_add_co_u32_e32 v6, vcc, s49, v62
	s_lshl_b64 s[18:19], s[18:19], 21
	s_nop 0
	v_addc_co_u32_e32 v7, vcc, 0, v63, vcc
	v_add_co_u32_e32 v10, vcc, s51, v62
	global_load_dwordx4 v[2:5], v[62:63], off nt
	s_nop 0
	global_load_dwordx4 v[6:9], v[6:7], off nt
	v_addc_co_u32_e32 v11, vcc, 0, v63, vcc
	v_add_co_u32_e32 v14, vcc, s53, v62
	s_add_u32 s17, s34, s18
	s_nop 0
	v_addc_co_u32_e32 v15, vcc, 0, v63, vcc
	global_load_dwordx4 v[10:13], v[10:11], off nt
	s_nop 0
	global_load_dwordx4 v[14:17], v[14:15], off nt
	v_add_co_u32_e32 v18, vcc, s55, v62
	s_addc_u32 s18, s35, s19
	s_nop 0
	v_addc_co_u32_e32 v19, vcc, 0, v63, vcc
	v_add_co_u32_e32 v22, vcc, s57, v62
	s_lshl_b32 s19, s21, 10
	s_nop 0
	v_addc_co_u32_e32 v23, vcc, 0, v63, vcc
	global_load_dwordx4 v[18:21], v[18:19], off nt
	s_nop 0
	global_load_dwordx4 v[22:25], v[22:23], off nt
	v_add_co_u32_e32 v26, vcc, s59, v62
	s_add_u32 s17, s17, s19
	s_nop 0
	v_addc_co_u32_e32 v27, vcc, 0, v63, vcc
	v_add_co_u32_e32 v30, vcc, s61, v62
	s_addc_u32 s19, s18, 0
	s_nop 0
	v_addc_co_u32_e32 v31, vcc, 0, v63, vcc
	global_load_dwordx4 v[26:29], v[26:27], off nt
	s_nop 0
	global_load_dwordx4 v[30:33], v[30:31], off nt
	v_add_co_u32_e32 v34, vcc, s63, v62
	s_add_u32 s18, s17, s2
	s_nop 0
	v_addc_co_u32_e32 v35, vcc, 0, v63, vcc
	v_add_co_u32_e32 v38, vcc, s64, v62
	s_addc_u32 s19, s19, 0
	s_nop 0
	v_addc_co_u32_e32 v39, vcc, 0, v63, vcc
	global_load_dwordx4 v[34:37], v[34:35], off nt
	s_nop 0
	global_load_dwordx4 v[38:41], v[38:39], off nt
	v_add_co_u32_e32 v42, vcc, s65, v62
	s_nop 1
	v_addc_co_u32_e32 v43, vcc, 0, v63, vcc
	v_add_co_u32_e32 v46, vcc, s66, v62
	s_nop 1
	v_addc_co_u32_e32 v47, vcc, 0, v63, vcc
	global_load_dwordx4 v[42:45], v[42:43], off nt
	s_nop 0
	global_load_dwordx4 v[46:49], v[46:47], off nt
	v_add_co_u32_e32 v50, vcc, s67, v62
	s_nop 1
	v_addc_co_u32_e32 v51, vcc, 0, v63, vcc
	global_load_dwordx4 v[50:53], v[50:51], off nt
	v_add_co_u32_e32 v54, vcc, s68, v62
	s_nop 1
	v_addc_co_u32_e32 v55, vcc, 0, v63, vcc
	global_load_dwordx4 v[54:57], v[54:55], off nt
	v_add_co_u32_e32 v58, vcc, s69, v62
	s_nop 1
	v_addc_co_u32_e32 v59, vcc, 0, v63, vcc
	global_load_dwordx4 v[58:61], v[58:59], off nt
	v_add_co_u32_e32 v62, vcc, s70, v62
	s_nop 1
	v_addc_co_u32_e32 v63, vcc, 0, v63, vcc
	global_load_dwordx4 v[62:65], v[62:63], off nt
	s_waitcnt vmcnt(15)
	ds_write2_b32 v71, v2, v3 offset1:1
	ds_write2_b32 v71, v4, v5 offset0:2 offset1:3
	v_add_u32_e32 v2, 0x420, v71
	s_waitcnt vmcnt(14)
	ds_write2_b32 v2, v6, v7 offset1:1
	v_add_u32_e32 v2, 0x428, v71
	ds_write2_b32 v2, v8, v9 offset1:1
	v_add_u32_e32 v2, 0x840, v71
	s_waitcnt vmcnt(13)
	ds_write2_b32 v2, v10, v11 offset1:1
	v_add_u32_e32 v2, 0x848, v71
	ds_write2_b32 v2, v12, v13 offset1:1
	v_add_u32_e32 v2, 0xc60, v71
	s_waitcnt vmcnt(12)
	ds_write2_b32 v2, v14, v15 offset1:1
	v_add_u32_e32 v2, 0xc68, v71
	ds_write2_b32 v2, v16, v17 offset1:1
	v_add_u32_e32 v2, 0x1080, v71
	s_waitcnt vmcnt(11)
	ds_write2_b32 v2, v18, v19 offset1:1
	v_add_u32_e32 v2, 0x1088, v71
	ds_write2_b32 v2, v20, v21 offset1:1
	v_add_u32_e32 v2, 0x14a0, v71
	s_waitcnt vmcnt(10)
	ds_write2_b32 v2, v22, v23 offset1:1
	v_add_u32_e32 v2, 0x14a8, v71
	ds_write2_b32 v2, v24, v25 offset1:1
	v_add_u32_e32 v2, 0x18c0, v71
	s_waitcnt vmcnt(9)
	ds_write2_b32 v2, v26, v27 offset1:1
	v_add_u32_e32 v2, 0x18c8, v71
	ds_write2_b32 v2, v28, v29 offset1:1
	v_add_u32_e32 v2, 0x1ce0, v71
	s_waitcnt vmcnt(8)
	ds_write2_b32 v2, v30, v31 offset1:1
	v_add_u32_e32 v2, 0x1ce8, v71
	ds_write2_b32 v2, v32, v33 offset1:1
	v_add_u32_e32 v2, 0x2100, v71
	s_waitcnt vmcnt(7)
	ds_write2_b32 v2, v34, v35 offset1:1
	v_add_u32_e32 v2, 0x2108, v71
	ds_write2_b32 v2, v36, v37 offset1:1
	v_add_u32_e32 v2, 0x2520, v71
	s_waitcnt vmcnt(6)
	ds_write2_b32 v2, v38, v39 offset1:1
	v_add_u32_e32 v2, 0x2528, v71
	ds_write2_b32 v2, v40, v41 offset1:1
	v_add_u32_e32 v2, 0x2940, v71
	v_lshl_add_u64 v[38:39], s[18:19], 0, v[68:69]
	v_lshl_add_u64 v[40:41], v[38:39], 0, v[108:109]
	s_waitcnt vmcnt(5)
	ds_write2_b32 v2, v42, v43 offset1:1
	v_add_u32_e32 v2, 0x2948, v71
	ds_write2_b32 v2, v44, v45 offset1:1
	v_add_u32_e32 v2, 0x2d60, v71
	s_waitcnt vmcnt(4)
	ds_write2_b32 v2, v46, v47 offset1:1
	v_add_u32_e32 v2, 0x2d68, v71
	ds_write2_b32 v2, v48, v49 offset1:1
	v_add_u32_e32 v2, 0x3180, v71
	s_waitcnt vmcnt(3)
	ds_write2_b32 v2, v50, v51 offset1:1
	v_add_u32_e32 v2, 0x3188, v71
	ds_write2_b32 v2, v52, v53 offset1:1
	v_add_u32_e32 v2, 0x35a0, v71
	v_add_u32_e32 v42, 0x400, v119
	s_waitcnt vmcnt(2)
	ds_write2_b32 v2, v54, v55 offset1:1
	v_add_u32_e32 v2, 0x35a8, v71
	ds_write2_b32 v2, v56, v57 offset1:1
	v_add_u32_e32 v2, 0x39c0, v71
	s_waitcnt vmcnt(1)
	ds_write2_b32 v2, v58, v59 offset1:1
	v_add_u32_e32 v2, 0x39c8, v71
	ds_write2_b32 v2, v60, v61 offset1:1
	v_add_u32_e32 v2, 0x3de0, v71
	s_waitcnt vmcnt(0)
	ds_write2_b32 v2, v62, v63 offset1:1
	v_add_u32_e32 v2, 0x3de8, v71
	ds_write2_b32 v2, v64, v65 offset1:1
	s_waitcnt lgkmcnt(0)
	ds_read2_b32 v[6:7], v119 offset0:66 offset1:74
	ds_read2_b32 v[8:9], v119 offset0:99 offset1:107
	ds_read2_b32 v[10:11], v119 offset1:8
	ds_read2_b32 v[12:13], v119 offset0:33 offset1:41
	v_mov_b32_e32 v2, v67
	s_waitcnt lgkmcnt(3)
	v_mul_f32_e32 v3, 0x42000000, v6
	ds_read2_b32 v[14:15], v119 offset0:198 offset1:206
	ds_read2_b32 v[16:17], v119 offset0:231 offset1:239
	ds_read2_b32 v[18:19], v119 offset0:132 offset1:140
	ds_read2_b32 v[20:21], v119 offset0:165 offset1:173
	s_waitcnt lgkmcnt(5)
	v_mul_f32_e32 v5, 0x42000000, v10
	s_waitcnt lgkmcnt(4)
	v_mul_f32_e32 v6, 0x42000000, v12
	v_cvt_pk_fp8_f32 v2, v5, v6
	v_mul_f32_e32 v4, 0x42000000, v8
	s_waitcnt lgkmcnt(1)
	v_mul_f32_e32 v6, 0x42000000, v18
	s_waitcnt lgkmcnt(0)
	v_mul_f32_e32 v8, 0x42000000, v20
	v_cvt_pk_fp8_f32 v2, v3, v4 op_sel:[0,0,1]
	v_mov_b32_e32 v3, v67
	ds_read2_b32 v[22:23], v42 offset0:74 offset1:82
	ds_read2_b32 v[24:25], v42 offset0:107 offset1:115
	ds_read2_b32 v[26:27], v42 offset0:8 offset1:16
	ds_read2_b32 v[28:29], v42 offset0:41 offset1:49
	v_cvt_pk_fp8_f32 v3, v6, v8
	ds_read2_b32 v[30:31], v42 offset0:140 offset1:148
	ds_read2_b32 v[32:33], v42 offset0:173 offset1:181
	v_mul_f32_e32 v4, 0x42000000, v14
	v_mul_f32_e32 v5, 0x42000000, v16
	v_cvt_pk_fp8_f32 v3, v4, v5 op_sel:[0,0,1]
	s_waitcnt lgkmcnt(3)
	v_mul_f32_e32 v5, 0x42000000, v26
	s_waitcnt lgkmcnt(2)
	v_mul_f32_e32 v10, 0x42000000, v28
	v_mov_b32_e32 v4, v67
	ds_read2_b32 v[34:35], v42 offset0:206 offset1:214
	ds_read2_b32 v[36:37], v42 offset0:239 offset1:247
	v_cvt_pk_fp8_f32 v4, v5, v10
	s_waitcnt lgkmcnt(3)
	v_mul_f32_e32 v10, 0x42000000, v30
	s_waitcnt lgkmcnt(2)
	v_mul_f32_e32 v12, 0x42000000, v32
	v_mov_b32_e32 v5, v67
	v_cvt_pk_fp8_f32 v5, v10, v12
	v_mul_f32_e32 v6, 0x42000000, v22
	v_mul_f32_e32 v8, 0x42000000, v24
	v_cvt_pk_fp8_f32 v4, v6, v8 op_sel:[0,0,1]
	s_waitcnt lgkmcnt(1)
	v_mul_f32_e32 v6, 0x42000000, v34
	s_waitcnt lgkmcnt(0)
	v_mul_f32_e32 v8, 0x42000000, v36
	v_cvt_pk_fp8_f32 v5, v6, v8 op_sel:[0,0,1]
	v_mul_f32_e32 v6, 0x42000000, v13
	v_mul_f32_e32 v8, 0x42000000, v29
	global_store_dwordx4 v[40:41], v[2:5], off
	s_nop 1
	v_mul_f32_e32 v3, 0x42000000, v11
	v_mov_b32_e32 v2, v67
	v_mul_f32_e32 v4, 0x42000000, v7
	v_cvt_pk_fp8_f32 v2, v3, v6
	v_mul_f32_e32 v6, 0x42000000, v19
	v_mul_f32_e32 v7, 0x42000000, v21
	v_mov_b32_e32 v3, v67
	v_cvt_pk_fp8_f32 v3, v6, v7
	v_mul_f32_e32 v5, 0x42000000, v9
	v_cvt_pk_fp8_f32 v2, v4, v5 op_sel:[0,0,1]
	v_mul_f32_e32 v4, 0x42000000, v15
	v_mul_f32_e32 v5, 0x42000000, v17
	v_cvt_pk_fp8_f32 v3, v4, v5 op_sel:[0,0,1]
	v_mul_f32_e32 v5, 0x42000000, v27
	v_mov_b32_e32 v4, v67
	v_cvt_pk_fp8_f32 v4, v5, v8
	v_mul_f32_e32 v8, 0x42000000, v31
	v_mul_f32_e32 v9, 0x42000000, v33
	v_mov_b32_e32 v5, v67
	v_cvt_pk_fp8_f32 v5, v8, v9
	v_mul_f32_e32 v6, 0x42000000, v23
	v_mul_f32_e32 v7, 0x42000000, v25
	v_cvt_pk_fp8_f32 v4, v6, v7 op_sel:[0,0,1]
	v_mul_f32_e32 v6, 0x42000000, v35
	v_mul_f32_e32 v7, 0x42000000, v37
	ds_read2_b32 v[8:9], v119 offset0:82 offset1:90
	ds_read2_b32 v[10:11], v119 offset0:115 offset1:123
	ds_read2_b32 v[12:13], v119 offset0:16 offset1:24
	ds_read2_b32 v[14:15], v119 offset0:49 offset1:57
	v_cvt_pk_fp8_f32 v5, v6, v7 op_sel:[0,0,1]
	v_lshl_add_u64 v[6:7], v[38:39], 0, v[72:73]
	global_store_dwordx4 v[6:7], v[2:5], off
	s_waitcnt lgkmcnt(1)
	s_nop 0
	v_mul_f32_e32 v5, 0x42000000, v12
	s_waitcnt lgkmcnt(0)
	v_mul_f32_e32 v6, 0x42000000, v14
	v_mov_b32_e32 v2, v67
	v_cvt_pk_fp8_f32 v2, v5, v6
	ds_read2_b32 v[16:17], v119 offset0:214 offset1:222
	ds_read2_b32 v[18:19], v119 offset0:247 offset1:255
	ds_read2_b32 v[6:7], v119 offset0:148 offset1:156
	ds_read2_b32 v[20:21], v119 offset0:181 offset1:189
	v_mul_f32_e32 v3, 0x42000000, v8
	v_mul_f32_e32 v4, 0x42000000, v10
	v_cvt_pk_fp8_f32 v2, v3, v4 op_sel:[0,0,1]
	s_waitcnt lgkmcnt(1)
	v_mul_f32_e32 v6, 0x42000000, v6
	s_waitcnt lgkmcnt(0)
	v_mul_f32_e32 v8, 0x42000000, v20
	v_mov_b32_e32 v3, v67
	ds_read2_b32 v[22:23], v42 offset0:90 offset1:98
	ds_read2_b32 v[24:25], v42 offset0:123 offset1:131
	ds_read2_b32 v[26:27], v42 offset0:24 offset1:32
	ds_read2_b32 v[28:29], v42 offset0:57 offset1:65
	v_cvt_pk_fp8_f32 v3, v6, v8
	v_mul_f32_e32 v4, 0x42000000, v16
	v_mul_f32_e32 v5, 0x42000000, v18
	ds_read2_b32 v[30:31], v42 offset0:156 offset1:164
	ds_read2_b32 v[32:33], v42 offset0:189 offset1:197
	ds_read2_b32 v[34:35], v42 offset0:222 offset1:230
	v_cvt_pk_fp8_f32 v3, v4, v5 op_sel:[0,0,1]
	s_waitcnt lgkmcnt(4)
	v_mul_f32_e32 v5, 0x42000000, v26
	s_waitcnt lgkmcnt(3)
	v_mul_f32_e32 v10, 0x42000000, v28
	v_mov_b32_e32 v4, v67
	v_cvt_pk_fp8_f32 v4, v5, v10
	v_add_u32_e32 v5, 0x600, v119
	ds_read2_b32 v[36:37], v5 offset0:127 offset1:135
	s_waitcnt lgkmcnt(3)
	v_mul_f32_e32 v10, 0x42000000, v30
	s_waitcnt lgkmcnt(2)
	v_mul_f32_e32 v12, 0x42000000, v32
	v_mov_b32_e32 v5, v67
	v_cvt_pk_fp8_f32 v5, v10, v12
	v_mul_f32_e32 v6, 0x42000000, v22
	v_mul_f32_e32 v8, 0x42000000, v24
	v_cvt_pk_fp8_f32 v4, v6, v8 op_sel:[0,0,1]
	s_waitcnt lgkmcnt(1)
	v_mul_f32_e32 v6, 0x42000000, v34
	s_waitcnt lgkmcnt(0)
	v_mul_f32_e32 v8, 0x42000000, v36
	v_cvt_pk_fp8_f32 v5, v6, v8 op_sel:[0,0,1]
	v_mul_f32_e32 v8, 0x42000000, v9
	v_mul_f32_e32 v9, 0x42000000, v11
	v_mul_f32_e32 v10, 0x42000000, v13
	v_mul_f32_e32 v11, 0x42000000, v15
	v_mov_b32_e32 v6, v67
	v_cvt_pk_fp8_f32 v6, v10, v11
	v_mul_f32_e32 v10, 0x42000000, v7
	v_mul_f32_e32 v11, 0x42000000, v21
	v_mov_b32_e32 v7, v67
	v_cvt_pk_fp8_f32 v7, v10, v11
	v_cvt_pk_fp8_f32 v6, v8, v9 op_sel:[0,0,1]
	v_mul_f32_e32 v8, 0x42000000, v17
	v_mul_f32_e32 v9, 0x42000000, v19
	v_cvt_pk_fp8_f32 v7, v8, v9 op_sel:[0,0,1]
	v_mul_f32_e32 v9, 0x42000000, v27
	v_mul_f32_e32 v12, 0x42000000, v29
	v_mov_b32_e32 v8, v67
	v_cvt_pk_fp8_f32 v8, v9, v12
	v_mul_f32_e32 v12, 0x42000000, v31
	v_mul_f32_e32 v13, 0x42000000, v33
	v_mov_b32_e32 v9, v67
	v_cvt_pk_fp8_f32 v9, v12, v13
	v_mul_f32_e32 v10, 0x42000000, v23
	v_mul_f32_e32 v11, 0x42000000, v25
	v_cvt_pk_fp8_f32 v8, v10, v11 op_sel:[0,0,1]
	v_mul_f32_e32 v10, 0x42000000, v35
	v_mul_f32_e32 v11, 0x42000000, v37
	v_cvt_pk_fp8_f32 v9, v10, v11 op_sel:[0,0,1]
	v_lshl_add_u64 v[10:11], v[38:39], 0, v[78:79]
	global_store_dwordx4 v[10:11], v[2:5], off
	s_nop 1
	v_lshl_add_u64 v[2:3], v[38:39], 0, v[84:85]
	global_store_dwordx4 v[2:3], v[6:9], off
	s_waitcnt lgkmcnt(0)

.LBB0_22:
	s_andn2_b64 vcc, exec, s[18:19]
	s_cbranch_vccnz .LBB0_24
	s_mul_i32 s2, s16, 0xfffe5c00
	s_add_i32 s2, s46, s2
	s_and_b32 s2, s2, 0x3fc0
	s_ashr_i32 s17, s16, 31
	s_addk_i32 s2, 0xe000
	s_lshl_b64 s[18:19], s[16:17], 22
	s_lshl_b64 s[22:23], s[2:3], 12
	s_waitcnt lgkmcnt(0)
	s_add_u32 s18, s10, s18
	s_addc_u32 s19, s11, s19
	s_add_u32 s18, s18, s22
	s_addc_u32 s19, s19, s23
	s_and_b32 s21, s45, 0x3c0
	s_lshl_b32 s22, s21, 2
	s_add_u32 s18, s18, s22
	s_addc_u32 s19, s19, 0
	v_lshlrev_b32_e32 v66, 2, v118
	v_lshl_add_u64 v[62:63], s[18:19], 0, v[66:67]
	v_lshl_add_u64 v[2:3], v[62:63], 0, v[120:121]
	global_load_dwordx4 v[2:5], v[2:3], off nt
	v_lshl_add_u64 v[34:35], v[62:63], 0, v[152:153]
	v_lshl_add_u64 v[38:39], v[62:63], 0, v[156:157]
	v_lshl_add_u64 v[6:7], v[62:63], 0, v[124:125]
	global_load_dwordx4 v[34:37], v[34:35], off nt
	v_lshl_add_u64 v[42:43], v[62:63], 0, v[160:161]
	global_load_dwordx4 v[38:41], v[38:39], off nt
	v_lshl_add_u64 v[10:11], v[62:63], 0, v[128:129]
	global_load_dwordx4 v[6:9], v[6:7], off nt
	v_lshl_add_u64 v[46:47], v[62:63], 0, v[164:165]
	global_load_dwordx4 v[42:45], v[42:43], off nt
	v_lshl_add_u64 v[14:15], v[62:63], 0, v[132:133]
	global_load_dwordx4 v[10:13], v[10:11], off nt
	v_lshl_add_u64 v[50:51], v[62:63], 0, v[168:169]
	global_load_dwordx4 v[46:49], v[46:47], off nt
	v_lshl_add_u64 v[18:19], v[62:63], 0, v[136:137]
	global_load_dwordx4 v[14:17], v[14:15], off nt
	v_lshl_add_u64 v[54:55], v[62:63], 0, v[172:173]
	global_load_dwordx4 v[50:53], v[50:51], off nt
	v_lshl_add_u64 v[22:23], v[62:63], 0, v[140:141]
	global_load_dwordx4 v[18:21], v[18:19], off nt
	v_lshl_add_u64 v[58:59], v[62:63], 0, v[176:177]
	global_load_dwordx4 v[54:57], v[54:55], off nt
	v_lshl_add_u64 v[26:27], v[62:63], 0, v[144:145]
	global_load_dwordx4 v[22:25], v[22:23], off nt
	v_lshl_add_u64 v[30:31], v[62:63], 0, v[148:149]
	global_load_dwordx4 v[58:61], v[58:59], off nt
	v_lshl_add_u64 v[62:63], v[62:63], 0, v[180:181]
	global_load_dwordx4 v[26:29], v[26:27], off nt
	v_add_u32_e32 v66, v189, v188
	global_load_dwordx4 v[62:65], v[62:63], off nt
	v_add_u32_e32 v186, 0x410, v66
	global_load_dwordx4 v[30:33], v[30:31], off nt
	v_add_u32_e32 v187, 0x418, v66
	v_add_u32_e32 v190, 0x820, v66
	v_add_u32_e32 v191, 0x828, v66
	v_add_u32_e32 v192, 0xc30, v66
	v_add_u32_e32 v193, 0xc38, v66
	v_add_u32_e32 v194, 0x1040, v66
	v_add_u32_e32 v195, 0x1048, v66
	v_add_u32_e32 v196, 0x1450, v66
	v_add_u32_e32 v197, 0x1458, v66
	v_add_u32_e32 v198, 0x1860, v66
	v_add_u32_e32 v199, 0x1868, v66
	v_add_u32_e32 v200, 0x1c70, v66
	v_add_u32_e32 v201, 0x1c78, v66
	v_add_u32_e32 v202, 0x2080, v66
	v_add_u32_e32 v203, 0x2088, v66
	v_add_u32_e32 v204, 0x2490, v66
	s_lshl_b64 s[18:19], s[16:17], 21
	s_add_u32 s17, s36, s18
	s_addc_u32 s18, s37, s19
	s_lshl_b32 s19, s21, 11
	s_add_u32 s17, s17, s19
	s_addc_u32 s21, s18, 0
	s_lshl_b64 s[18:19], s[2:3], 1
	s_add_u32 s18, s17, s18
	s_addc_u32 s19, s21, s19
	s_waitcnt vmcnt(15)
	ds_write2_b32 v66, v2, v3 offset1:1
	ds_write2_b32 v66, v4, v5 offset0:2 offset1:3
	s_waitcnt vmcnt(12)
	ds_write2_b32 v186, v6, v7 offset1:1
	ds_write2_b32 v187, v8, v9 offset1:1
	s_waitcnt vmcnt(10)
	ds_write2_b32 v190, v10, v11 offset1:1
	ds_write2_b32 v191, v12, v13 offset1:1
	s_waitcnt vmcnt(8)
	ds_write2_b32 v192, v14, v15 offset1:1
	ds_write2_b32 v193, v16, v17 offset1:1
	s_waitcnt vmcnt(6)
	ds_write2_b32 v194, v18, v19 offset1:1
	ds_write2_b32 v195, v20, v21 offset1:1
	s_waitcnt vmcnt(4)
	ds_write2_b32 v196, v22, v23 offset1:1
	ds_write2_b32 v197, v24, v25 offset1:1
	s_waitcnt vmcnt(2)
	ds_write2_b32 v198, v26, v27 offset1:1
	ds_write2_b32 v199, v28, v29 offset1:1
	s_waitcnt vmcnt(0)
	ds_write2_b32 v200, v30, v31 offset1:1
	ds_write2_b32 v201, v32, v33 offset1:1
	ds_write2_b32 v202, v34, v35 offset1:1
	ds_write2_b32 v203, v36, v37 offset1:1
	ds_write2_b32 v204, v38, v39 offset1:1
	v_add_u32_e32 v2, 0x2498, v66
	ds_write2_b32 v2, v40, v41 offset1:1
	v_add_u32_e32 v2, 0x28a0, v66
	ds_write2_b32 v2, v42, v43 offset1:1
	v_add_u32_e32 v2, 0x28a8, v66
	ds_write2_b32 v2, v44, v45 offset1:1
	v_add_u32_e32 v2, 0x2cb0, v66
	ds_write2_b32 v2, v46, v47 offset1:1
	v_add_u32_e32 v2, 0x2cb8, v66
	ds_write2_b32 v2, v48, v49 offset1:1
	v_add_u32_e32 v2, 0x30c0, v66
	ds_write2_b32 v2, v50, v51 offset1:1
	v_add_u32_e32 v2, 0x30c8, v66
	ds_write2_b32 v2, v52, v53 offset1:1
	v_add_u32_e32 v2, 0x34d0, v66
	ds_write2_b32 v2, v54, v55 offset1:1
	v_add_u32_e32 v2, 0x34d8, v66
	ds_write2_b32 v2, v56, v57 offset1:1
	v_add_u32_e32 v2, 0x38e0, v66
	ds_write2_b32 v2, v58, v59 offset1:1
	v_add_u32_e32 v2, 0x38e8, v66
	ds_write2_b32 v2, v60, v61 offset1:1
	v_add_u32_e32 v2, 0x3cf0, v66
	ds_write2_b32 v2, v62, v63 offset1:1
	v_add_u32_e32 v2, 0x3cf8, v66
	ds_write2_b32 v2, v64, v65 offset1:1
	s_waitcnt lgkmcnt(0)
	v_add_u32_e32 v26, 0x400, v185
	ds_read2_b32 v[6:7], v185 offset0:65 offset1:73
	ds_read2_b32 v[8:9], v185 offset1:8
	ds_read2_b32 v[10:11], v185 offset0:130 offset1:138
	ds_read2_b32 v[12:13], v185 offset0:195 offset1:203
	ds_read2_b32 v[14:15], v26 offset0:4 offset1:12
	ds_read2_b32 v[16:17], v26 offset0:69 offset1:77
	ds_read2_b32 v[18:19], v26 offset0:134 offset1:142
	ds_read2_b32 v[20:21], v26 offset0:199 offset1:207
	v_lshlrev_b32_e32 v66, 1, v70
	v_lshl_add_u64 v[22:23], s[18:19], 0, v[66:67]
	s_waitcnt lgkmcnt(6)
	v_cvt_pk_bf16_f32 v2, v8, v6
	s_waitcnt lgkmcnt(4)
	v_cvt_pk_bf16_f32 v3, v10, v12
	s_waitcnt lgkmcnt(2)
	v_cvt_pk_bf16_f32 v4, v14, v16
	s_waitcnt lgkmcnt(0)
	v_cvt_pk_bf16_f32 v5, v18, v20
	v_lshl_add_u64 v[24:25], v[22:23], 0, v[112:113]
	global_store_dwordx4 v[24:25], v[2:5], off
	s_nop 1
	v_cvt_pk_bf16_f32 v2, v9, v7
	v_cvt_pk_bf16_f32 v3, v11, v13
	v_cvt_pk_bf16_f32 v4, v15, v17
	v_cvt_pk_bf16_f32 v5, v19, v21
	ds_read2_b32 v[8:9], v185 offset0:81 offset1:89
	ds_read2_b32 v[10:11], v185 offset0:16 offset1:24
	ds_read2_b32 v[12:13], v185 offset0:146 offset1:154
	ds_read2_b32 v[14:15], v185 offset0:211 offset1:219
	ds_read2_b32 v[16:17], v26 offset0:20 offset1:28
	ds_read2_b32 v[18:19], v26 offset0:85 offset1:93
	ds_read2_b32 v[20:21], v26 offset0:150 offset1:158
	ds_read2_b32 v[24:25], v26 offset0:215 offset1:223
	v_lshl_add_u64 v[6:7], v[22:23], 0, v[74:75]
	global_store_dwordx4 v[6:7], v[2:5], off
	v_lshl_add_u64 v[6:7], v[22:23], 0, v[80:81]
	s_waitcnt lgkmcnt(6)
	v_cvt_pk_bf16_f32 v2, v10, v8
	s_waitcnt lgkmcnt(4)
	v_cvt_pk_bf16_f32 v3, v12, v14
	s_waitcnt lgkmcnt(2)
	v_cvt_pk_bf16_f32 v4, v16, v18
	s_waitcnt lgkmcnt(0)
	v_cvt_pk_bf16_f32 v5, v20, v24
	global_store_dwordx4 v[6:7], v[2:5], off
	v_lshl_add_u64 v[6:7], v[22:23], 0, v[86:87]
	s_nop 0
	v_cvt_pk_bf16_f32 v2, v11, v9
	v_cvt_pk_bf16_f32 v3, v13, v15
	v_cvt_pk_bf16_f32 v4, v17, v19
	v_cvt_pk_bf16_f32 v5, v21, v25
	ds_read2_b32 v[8:9], v185 offset0:32 offset1:40
	ds_read2_b32 v[10:11], v185 offset0:97 offset1:105
	ds_read2_b32 v[12:13], v185 offset0:162 offset1:170
	ds_read2_b32 v[14:15], v185 offset0:227 offset1:235
	ds_read2_b32 v[16:17], v26 offset0:36 offset1:44
	ds_read2_b32 v[18:19], v26 offset0:101 offset1:109
	ds_read2_b32 v[20:21], v26 offset0:166 offset1:174
	ds_read2_b32 v[24:25], v26 offset0:231 offset1:239
	global_store_dwordx4 v[6:7], v[2:5], off
	v_lshl_add_u64 v[6:7], v[22:23], 0, v[90:91]
	s_waitcnt lgkmcnt(6)
	v_cvt_pk_bf16_f32 v2, v8, v10
	s_waitcnt lgkmcnt(4)
	v_cvt_pk_bf16_f32 v3, v12, v14
	s_waitcnt lgkmcnt(2)
	v_cvt_pk_bf16_f32 v4, v16, v18
	s_waitcnt lgkmcnt(0)
	v_cvt_pk_bf16_f32 v5, v20, v24
	global_store_dwordx4 v[6:7], v[2:5], off
	v_lshl_add_u64 v[6:7], v[22:23], 0, v[94:95]
	s_nop 0
	v_cvt_pk_bf16_f32 v2, v9, v11
	v_cvt_pk_bf16_f32 v3, v13, v15
	v_cvt_pk_bf16_f32 v4, v17, v19
	v_cvt_pk_bf16_f32 v5, v21, v25
	ds_read2_b32 v[8:9], v185 offset0:48 offset1:56
	ds_read2_b32 v[10:11], v185 offset0:113 offset1:121
	ds_read2_b32 v[12:13], v185 offset0:178 offset1:186
	ds_read2_b32 v[14:15], v185 offset0:243 offset1:251
	ds_read2_b32 v[16:17], v26 offset0:52 offset1:60
	ds_read2_b32 v[18:19], v26 offset0:117 offset1:125
	ds_read2_b32 v[20:21], v26 offset0:182 offset1:190
	ds_read2_b32 v[24:25], v26 offset0:247 offset1:255
	global_store_dwordx4 v[6:7], v[2:5], off
	v_lshl_add_u64 v[6:7], v[22:23], 0, v[98:99]
	s_waitcnt lgkmcnt(6)
	v_cvt_pk_bf16_f32 v2, v8, v10
	s_waitcnt lgkmcnt(4)
	v_cvt_pk_bf16_f32 v3, v12, v14
	s_waitcnt lgkmcnt(2)
	v_cvt_pk_bf16_f32 v4, v16, v18
	s_waitcnt lgkmcnt(0)
	v_cvt_pk_bf16_f32 v5, v20, v24
	global_store_dwordx4 v[6:7], v[2:5], off
	v_lshl_add_u64 v[6:7], v[22:23], 0, v[102:103]
	s_nop 0
	v_cvt_pk_bf16_f32 v2, v9, v11
	v_cvt_pk_bf16_f32 v3, v13, v15
	v_cvt_pk_bf16_f32 v4, v17, v19
	v_cvt_pk_bf16_f32 v5, v21, v25
	global_store_dwordx4 v[6:7], v[2:5], off
	s_waitcnt lgkmcnt(0)

.LBB0_25:
	s_andn2_b64 vcc, exec, s[18:19]
	s_cbranch_vccnz .LBB0_27
	s_add_i32 s2, s20, 0xfffff900
	s_lshr_b32 s2, s2, 6
	s_lshl_b32 s17, s16, 2
	s_add_i32 s18, s2, s17
	s_ashr_i32 s19, s18, 31
	s_and_b32 s2, s46, 0xc0
	s_lshl_b64 s[22:23], s[18:19], 20
	s_waitcnt lgkmcnt(0)
	s_add_u32 s17, s8, s22
	s_addc_u32 s21, s9, s23
	s_lshl_b32 s22, s2, 12
	s_add_u32 s17, s17, s22
	s_addc_u32 s21, s21, 0
	s_and_b32 s24, s45, 0x3c0
	s_lshl_b32 s22, s24, 2
	s_add_u32 s22, s17, s22
	s_addc_u32 s23, s21, 0
	v_lshlrev_b32_e32 v66, 2, v118
	v_lshl_add_u64 v[62:63], s[22:23], 0, v[66:67]
	v_lshl_add_u64 v[2:3], v[62:63], 0, v[120:121]
	global_load_dwordx4 v[2:5], v[2:3], off nt
	v_lshl_add_u64 v[34:35], v[62:63], 0, v[152:153]
	v_lshl_add_u64 v[38:39], v[62:63], 0, v[156:157]
	v_lshl_add_u64 v[6:7], v[62:63], 0, v[124:125]
	global_load_dwordx4 v[34:37], v[34:35], off nt
	v_lshl_add_u64 v[42:43], v[62:63], 0, v[160:161]
	global_load_dwordx4 v[38:41], v[38:39], off nt
	v_lshl_add_u64 v[10:11], v[62:63], 0, v[128:129]
	global_load_dwordx4 v[6:9], v[6:7], off nt
	v_lshl_add_u64 v[46:47], v[62:63], 0, v[164:165]
	global_load_dwordx4 v[42:45], v[42:43], off nt
	v_lshl_add_u64 v[14:15], v[62:63], 0, v[132:133]
	global_load_dwordx4 v[10:13], v[10:11], off nt
	v_lshl_add_u64 v[50:51], v[62:63], 0, v[168:169]
	global_load_dwordx4 v[46:49], v[46:47], off nt
	v_lshl_add_u64 v[18:19], v[62:63], 0, v[136:137]
	global_load_dwordx4 v[14:17], v[14:15], off nt
	v_lshl_add_u64 v[54:55], v[62:63], 0, v[172:173]
	global_load_dwordx4 v[50:53], v[50:51], off nt
	v_lshl_add_u64 v[22:23], v[62:63], 0, v[140:141]
	global_load_dwordx4 v[18:21], v[18:19], off nt
	v_lshl_add_u64 v[58:59], v[62:63], 0, v[176:177]
	global_load_dwordx4 v[54:57], v[54:55], off nt
	v_lshl_add_u64 v[26:27], v[62:63], 0, v[144:145]
	global_load_dwordx4 v[22:25], v[22:23], off nt
	v_lshl_add_u64 v[30:31], v[62:63], 0, v[148:149]
	global_load_dwordx4 v[58:61], v[58:59], off nt
	v_lshl_add_u64 v[62:63], v[62:63], 0, v[180:181]
	global_load_dwordx4 v[26:29], v[26:27], off nt
	v_add_u32_e32 v66, v189, v188
	global_load_dwordx4 v[62:65], v[62:63], off nt
	v_add_u32_e32 v186, 0x410, v66
	global_load_dwordx4 v[30:33], v[30:31], off nt
	v_add_u32_e32 v187, 0x418, v66
	v_add_u32_e32 v190, 0x820, v66
	v_add_u32_e32 v191, 0x828, v66
	v_add_u32_e32 v192, 0xc30, v66
	v_add_u32_e32 v193, 0xc38, v66
	v_add_u32_e32 v194, 0x1040, v66
	v_add_u32_e32 v195, 0x1048, v66
	v_add_u32_e32 v196, 0x1450, v66
	v_add_u32_e32 v197, 0x1458, v66
	v_add_u32_e32 v198, 0x1860, v66
	v_add_u32_e32 v199, 0x1868, v66
	v_add_u32_e32 v200, 0x1c70, v66
	v_add_u32_e32 v201, 0x1c78, v66
	v_add_u32_e32 v202, 0x2080, v66
	v_add_u32_e32 v203, 0x2088, v66
	v_add_u32_e32 v204, 0x2490, v66
	s_lshl_b64 s[18:19], s[18:19], 19
	s_add_u32 s17, s38, s18
	s_addc_u32 s18, s39, s19
	s_lshl_b32 s19, s24, 9
	s_add_u32 s17, s17, s19
	s_addc_u32 s19, s18, 0
	s_lshl_b32 s2, s2, 1
	s_add_u32 s18, s17, s2
	s_addc_u32 s19, s19, 0
	s_waitcnt vmcnt(15)
	ds_write2_b32 v66, v2, v3 offset1:1
	ds_write2_b32 v66, v4, v5 offset0:2 offset1:3
	s_waitcnt vmcnt(12)
	ds_write2_b32 v186, v6, v7 offset1:1
	ds_write2_b32 v187, v8, v9 offset1:1
	s_waitcnt vmcnt(10)
	ds_write2_b32 v190, v10, v11 offset1:1
	ds_write2_b32 v191, v12, v13 offset1:1
	s_waitcnt vmcnt(8)
	ds_write2_b32 v192, v14, v15 offset1:1
	ds_write2_b32 v193, v16, v17 offset1:1
	s_waitcnt vmcnt(6)
	ds_write2_b32 v194, v18, v19 offset1:1
	ds_write2_b32 v195, v20, v21 offset1:1
	s_waitcnt vmcnt(4)
	ds_write2_b32 v196, v22, v23 offset1:1
	ds_write2_b32 v197, v24, v25 offset1:1
	s_waitcnt vmcnt(2)
	ds_write2_b32 v198, v26, v27 offset1:1
	ds_write2_b32 v199, v28, v29 offset1:1
	s_waitcnt vmcnt(0)
	ds_write2_b32 v200, v30, v31 offset1:1
	ds_write2_b32 v201, v32, v33 offset1:1
	ds_write2_b32 v202, v34, v35 offset1:1
	ds_write2_b32 v203, v36, v37 offset1:1
	ds_write2_b32 v204, v38, v39 offset1:1
	v_add_u32_e32 v2, 0x2498, v66
	ds_write2_b32 v2, v40, v41 offset1:1
	v_add_u32_e32 v2, 0x28a0, v66
	ds_write2_b32 v2, v42, v43 offset1:1
	v_add_u32_e32 v2, 0x28a8, v66
	ds_write2_b32 v2, v44, v45 offset1:1
	v_add_u32_e32 v2, 0x2cb0, v66
	ds_write2_b32 v2, v46, v47 offset1:1
	v_add_u32_e32 v2, 0x2cb8, v66
	ds_write2_b32 v2, v48, v49 offset1:1
	v_add_u32_e32 v2, 0x30c0, v66
	ds_write2_b32 v2, v50, v51 offset1:1
	v_add_u32_e32 v2, 0x30c8, v66
	ds_write2_b32 v2, v52, v53 offset1:1
	v_add_u32_e32 v2, 0x34d0, v66
	ds_write2_b32 v2, v54, v55 offset1:1
	v_add_u32_e32 v2, 0x34d8, v66
	ds_write2_b32 v2, v56, v57 offset1:1
	v_add_u32_e32 v2, 0x38e0, v66
	ds_write2_b32 v2, v58, v59 offset1:1
	v_add_u32_e32 v2, 0x38e8, v66
	ds_write2_b32 v2, v60, v61 offset1:1
	v_add_u32_e32 v2, 0x3cf0, v66
	ds_write2_b32 v2, v62, v63 offset1:1
	v_add_u32_e32 v2, 0x3cf8, v66
	ds_write2_b32 v2, v64, v65 offset1:1
	s_waitcnt lgkmcnt(0)
	v_add_u32_e32 v26, 0x400, v185
	ds_read2_b32 v[6:7], v185 offset0:65 offset1:73
	ds_read2_b32 v[8:9], v185 offset1:8
	ds_read2_b32 v[10:11], v185 offset0:130 offset1:138
	ds_read2_b32 v[12:13], v185 offset0:195 offset1:203
	ds_read2_b32 v[14:15], v26 offset0:4 offset1:12
	ds_read2_b32 v[16:17], v26 offset0:69 offset1:77
	ds_read2_b32 v[18:19], v26 offset0:134 offset1:142
	ds_read2_b32 v[20:21], v26 offset0:199 offset1:207
	v_lshlrev_b32_e32 v66, 1, v70
	v_lshl_add_u64 v[22:23], s[18:19], 0, v[66:67]
	s_waitcnt lgkmcnt(6)
	v_cvt_pk_bf16_f32 v2, v8, v6
	s_waitcnt lgkmcnt(4)
	v_cvt_pk_bf16_f32 v3, v10, v12
	s_waitcnt lgkmcnt(2)
	v_cvt_pk_bf16_f32 v4, v14, v16
	s_waitcnt lgkmcnt(0)
	v_cvt_pk_bf16_f32 v5, v18, v20
	v_lshl_add_u64 v[24:25], v[22:23], 0, v[114:115]
	global_store_dwordx4 v[24:25], v[2:5], off
	s_nop 1
	v_cvt_pk_bf16_f32 v2, v9, v7
	v_cvt_pk_bf16_f32 v3, v11, v13
	v_cvt_pk_bf16_f32 v4, v15, v17
	v_cvt_pk_bf16_f32 v5, v19, v21
	ds_read2_b32 v[8:9], v185 offset0:81 offset1:89
	ds_read2_b32 v[10:11], v185 offset0:16 offset1:24
	ds_read2_b32 v[12:13], v185 offset0:146 offset1:154
	ds_read2_b32 v[14:15], v185 offset0:211 offset1:219
	ds_read2_b32 v[16:17], v26 offset0:20 offset1:28
	ds_read2_b32 v[18:19], v26 offset0:85 offset1:93
	ds_read2_b32 v[20:21], v26 offset0:150 offset1:158
	ds_read2_b32 v[24:25], v26 offset0:215 offset1:223
	v_lshl_add_u64 v[6:7], v[22:23], 0, v[76:77]
	global_store_dwordx4 v[6:7], v[2:5], off
	v_lshl_add_u64 v[6:7], v[22:23], 0, v[82:83]
	s_waitcnt lgkmcnt(6)
	v_cvt_pk_bf16_f32 v2, v10, v8
	s_waitcnt lgkmcnt(4)
	v_cvt_pk_bf16_f32 v3, v12, v14
	s_waitcnt lgkmcnt(2)
	v_cvt_pk_bf16_f32 v4, v16, v18
	s_waitcnt lgkmcnt(0)
	v_cvt_pk_bf16_f32 v5, v20, v24
	global_store_dwordx4 v[6:7], v[2:5], off
	v_lshl_add_u64 v[6:7], v[22:23], 0, v[88:89]
	s_nop 0
	v_cvt_pk_bf16_f32 v2, v11, v9
	v_cvt_pk_bf16_f32 v3, v13, v15
	v_cvt_pk_bf16_f32 v4, v17, v19
	v_cvt_pk_bf16_f32 v5, v21, v25
	ds_read2_b32 v[8:9], v185 offset0:32 offset1:40
	ds_read2_b32 v[10:11], v185 offset0:97 offset1:105
	ds_read2_b32 v[12:13], v185 offset0:162 offset1:170
	ds_read2_b32 v[14:15], v185 offset0:227 offset1:235
	ds_read2_b32 v[16:17], v26 offset0:36 offset1:44
	ds_read2_b32 v[18:19], v26 offset0:101 offset1:109
	ds_read2_b32 v[20:21], v26 offset0:166 offset1:174
	ds_read2_b32 v[24:25], v26 offset0:231 offset1:239
	global_store_dwordx4 v[6:7], v[2:5], off
	v_lshl_add_u64 v[6:7], v[22:23], 0, v[92:93]
	s_waitcnt lgkmcnt(6)
	v_cvt_pk_bf16_f32 v2, v8, v10
	s_waitcnt lgkmcnt(4)
	v_cvt_pk_bf16_f32 v3, v12, v14
	s_waitcnt lgkmcnt(2)
	v_cvt_pk_bf16_f32 v4, v16, v18
	s_waitcnt lgkmcnt(0)
	v_cvt_pk_bf16_f32 v5, v20, v24
	global_store_dwordx4 v[6:7], v[2:5], off
	v_lshl_add_u64 v[6:7], v[22:23], 0, v[96:97]
	s_nop 0
	v_cvt_pk_bf16_f32 v2, v9, v11
	v_cvt_pk_bf16_f32 v3, v13, v15
	v_cvt_pk_bf16_f32 v4, v17, v19
	v_cvt_pk_bf16_f32 v5, v21, v25
	ds_read2_b32 v[8:9], v185 offset0:48 offset1:56
	ds_read2_b32 v[10:11], v185 offset0:113 offset1:121
	ds_read2_b32 v[12:13], v185 offset0:178 offset1:186
	ds_read2_b32 v[14:15], v185 offset0:243 offset1:251
	ds_read2_b32 v[16:17], v26 offset0:52 offset1:60
	ds_read2_b32 v[18:19], v26 offset0:117 offset1:125
	ds_read2_b32 v[20:21], v26 offset0:182 offset1:190
	ds_read2_b32 v[24:25], v26 offset0:247 offset1:255
	global_store_dwordx4 v[6:7], v[2:5], off
	v_lshl_add_u64 v[6:7], v[22:23], 0, v[100:101]
	s_waitcnt lgkmcnt(6)
	v_cvt_pk_bf16_f32 v2, v8, v10
	s_waitcnt lgkmcnt(4)
	v_cvt_pk_bf16_f32 v3, v12, v14
	s_waitcnt lgkmcnt(2)
	v_cvt_pk_bf16_f32 v4, v16, v18
	s_waitcnt lgkmcnt(0)
	v_cvt_pk_bf16_f32 v5, v20, v24
	global_store_dwordx4 v[6:7], v[2:5], off
	v_lshl_add_u64 v[6:7], v[22:23], 0, v[104:105]
	s_nop 0
	v_cvt_pk_bf16_f32 v2, v9, v11
	v_cvt_pk_bf16_f32 v3, v13, v15
	v_cvt_pk_bf16_f32 v4, v17, v19
	v_cvt_pk_bf16_f32 v5, v21, v25
	global_store_dwordx4 v[6:7], v[2:5], off
	s_waitcnt lgkmcnt(0)

.LBB0_28:
	s_andn2_b64 vcc, exec, s[18:19]
	s_cbranch_vccnz .LBB0_13
	s_mul_hi_i32 s2, s20, 0x92492493
	s_add_i32 s2, s2, s20
	s_lshr_b32 s17, s2, 31
	s_ashr_i32 s19, s2, 6
	s_add_i32 s19, s19, s17
	s_mul_i32 s2, s19, 0xffffff90
	s_mul_i32 s17, s16, 0x6900
	s_sub_i32 s2, s2, s17
	s_add_i32 s86, s30, s2
	s_lshl_b32 s18, s86, 6
	s_add_i32 s2, s18, 0xffffff10
	s_cmp_gt_u32 s86, 47
	s_cselect_b32 s2, s2, 0
	s_cmp_eq_u32 s86, 44
	s_cselect_b64 s[20:21], -1, 0
	s_and_b64 s[22:23], s[20:21], exec
	s_cselect_b32 s22, 0xb00, s2
	s_mov_b64 s[24:25], -1
	s_cmp_gt_i32 s86, 47
	s_mul_hi_i32 s87, s16, 0x1b10000
	s_mul_i32 s88, s16, 0x1b10000
	s_cbranch_scc0 .LBB0_31
	s_lshl_b32 s2, s19, 6
	s_and_b32 s25, s2, 0xffffff80
	s_lshl_b32 s2, s19, 5
	s_and_b32 s2, s2, 32
	s_ashr_i32 s17, s16, 31
	s_waitcnt lgkmcnt(0)
	s_add_u32 s23, s14, s88
	s_addc_u32 s89, s15, s87
	s_ashr_i32 s24, s25, 31
	s_mul_i32 s91, s25, 0x6c40
	s_mul_hi_i32 s90, s25, 0x6c40
	s_add_u32 s96, s23, s91
	s_addc_u32 s89, s89, s90
	s_ashr_i32 s23, s22, 31
	s_lshl_b64 s[90:91], s[22:23], 2
	s_add_u32 s23, s96, s90
	s_addc_u32 s89, s89, s91
	s_lshl_b32 s90, s2, 2
	s_add_u32 s90, s23, s90
	s_addc_u32 s91, s89, 0
	v_lshl_add_u64 v[2:3], s[90:91], 0, v[116:117]
	v_lshlrev_b32_e32 v66, 2, v184
	v_lshl_add_u64 v[62:63], v[2:3], 0, v[66:67]
	v_add_co_u32_e32 v6, vcc, s71, v62
	s_lshl_b64 s[90:91], s[16:17], 22
	s_nop 0
	v_addc_co_u32_e32 v7, vcc, 0, v63, vcc
	v_add_co_u32_e32 v10, vcc, s72, v62
	global_load_dwordx4 v[2:5], v[62:63], off nt
	s_nop 0
	global_load_dwordx4 v[6:9], v[6:7], off offset:512 nt
	v_addc_co_u32_e32 v11, vcc, 0, v63, vcc
	v_add_co_u32_e32 v14, vcc, s73, v62
	s_add_u32 s17, s40, s90
	s_nop 0
	v_addc_co_u32_e32 v15, vcc, 0, v63, vcc
	global_load_dwordx4 v[10:13], v[10:11], off offset:1024 nt
	s_nop 0
	global_load_dwordx4 v[14:17], v[14:15], off offset:1536 nt
	v_add_co_u32_e32 v18, vcc, s74, v62
	s_addc_u32 s23, s41, s91
	s_nop 0
	v_addc_co_u32_e32 v19, vcc, 0, v63, vcc
	v_add_co_u32_e32 v22, vcc, s75, v62
	s_add_i32 s2, s18, s2
	s_nop 0
	v_addc_co_u32_e32 v23, vcc, 0, v63, vcc
	global_load_dwordx4 v[18:21], v[18:19], off offset:2048 nt
	s_nop 0
	global_load_dwordx4 v[22:25], v[22:23], off offset:2560 nt
	v_add_co_u32_e32 v26, vcc, s76, v62
	s_addk_i32 s2, 0xf400
	s_nop 0
	v_addc_co_u32_e32 v27, vcc, 0, v63, vcc
	v_add_co_u32_e32 v30, vcc, s77, v62
	s_lshl_b64 s[90:91], s[2:3], 10
	s_nop 0
	v_addc_co_u32_e32 v31, vcc, 0, v63, vcc
	global_load_dwordx4 v[26:29], v[26:27], off offset:3072 nt
	s_nop 0
	global_load_dwordx4 v[30:33], v[30:31], off offset:3584 nt
	v_add_co_u32_e32 v34, vcc, s78, v62
	s_add_u32 s2, s17, s90
	s_nop 0
	v_addc_co_u32_e32 v35, vcc, 0, v63, vcc
	v_add_co_u32_e32 v38, vcc, s79, v62
	s_addc_u32 s17, s23, s91
	s_nop 0
	v_addc_co_u32_e32 v39, vcc, 0, v63, vcc
	global_load_dwordx4 v[34:37], v[34:35], off nt
	s_nop 0
	global_load_dwordx4 v[38:41], v[38:39], off offset:512 nt
	v_add_co_u32_e32 v42, vcc, s80, v62
	s_add_u32 s90, s2, s25
	s_nop 0
	v_addc_co_u32_e32 v43, vcc, 0, v63, vcc
	v_add_co_u32_e32 v46, vcc, s81, v62
	s_addc_u32 s91, s17, s24
	s_nop 0
	v_addc_co_u32_e32 v47, vcc, 0, v63, vcc
	global_load_dwordx4 v[42:45], v[42:43], off offset:1024 nt
	s_nop 0
	global_load_dwordx4 v[46:49], v[46:47], off offset:1536 nt
	v_add_co_u32_e32 v50, vcc, s82, v62
	s_mov_b64 s[24:25], 0
	s_nop 0
	v_addc_co_u32_e32 v51, vcc, 0, v63, vcc
	global_load_dwordx4 v[50:53], v[50:51], off offset:2048 nt
	v_add_co_u32_e32 v54, vcc, s83, v62
	s_nop 1
	v_addc_co_u32_e32 v55, vcc, 0, v63, vcc
	global_load_dwordx4 v[54:57], v[54:55], off offset:2560 nt
	v_add_co_u32_e32 v58, vcc, s84, v62
	s_nop 1
	v_addc_co_u32_e32 v59, vcc, 0, v63, vcc
	global_load_dwordx4 v[58:61], v[58:59], off offset:3072 nt
	v_add_co_u32_e32 v62, vcc, s85, v62
	s_nop 1
	v_addc_co_u32_e32 v63, vcc, 0, v63, vcc
	global_load_dwordx4 v[62:65], v[62:63], off offset:3584 nt
	s_waitcnt vmcnt(15)
	ds_write2_b32 v71, v2, v3 offset1:1
	ds_write2_b32 v71, v4, v5 offset0:2 offset1:3
	v_add_u32_e32 v2, 0x420, v71
	s_waitcnt vmcnt(14)
	ds_write2_b32 v2, v6, v7 offset1:1
	v_add_u32_e32 v2, 0x428, v71
	ds_write2_b32 v2, v8, v9 offset1:1
	v_add_u32_e32 v2, 0x840, v71
	s_waitcnt vmcnt(13)
	ds_write2_b32 v2, v10, v11 offset1:1
	v_add_u32_e32 v2, 0x848, v71
	ds_write2_b32 v2, v12, v13 offset1:1
	v_add_u32_e32 v2, 0xc60, v71
	s_waitcnt vmcnt(12)
	ds_write2_b32 v2, v14, v15 offset1:1
	v_add_u32_e32 v2, 0xc68, v71
	ds_write2_b32 v2, v16, v17 offset1:1
	v_add_u32_e32 v2, 0x1080, v71
	s_waitcnt vmcnt(11)
	ds_write2_b32 v2, v18, v19 offset1:1
	v_add_u32_e32 v2, 0x1088, v71
	ds_write2_b32 v2, v20, v21 offset1:1
	v_add_u32_e32 v2, 0x14a0, v71
	s_waitcnt vmcnt(10)
	ds_write2_b32 v2, v22, v23 offset1:1
	v_add_u32_e32 v2, 0x14a8, v71
	ds_write2_b32 v2, v24, v25 offset1:1
	v_add_u32_e32 v2, 0x18c0, v71
	s_waitcnt vmcnt(9)
	ds_write2_b32 v2, v26, v27 offset1:1
	v_add_u32_e32 v2, 0x18c8, v71
	ds_write2_b32 v2, v28, v29 offset1:1
	v_add_u32_e32 v2, 0x1ce0, v71
	s_waitcnt vmcnt(8)
	ds_write2_b32 v2, v30, v31 offset1:1
	v_add_u32_e32 v2, 0x1ce8, v71
	ds_write2_b32 v2, v32, v33 offset1:1
	v_add_u32_e32 v2, 0x2100, v71
	s_waitcnt vmcnt(7)
	ds_write2_b32 v2, v34, v35 offset1:1
	v_add_u32_e32 v2, 0x2108, v71
	ds_write2_b32 v2, v36, v37 offset1:1
	v_add_u32_e32 v2, 0x2520, v71
	s_waitcnt vmcnt(6)
	ds_write2_b32 v2, v38, v39 offset1:1
	v_add_u32_e32 v2, 0x2528, v71
	ds_write2_b32 v2, v40, v41 offset1:1
	v_add_u32_e32 v2, 0x2940, v71
	v_lshl_add_u64 v[38:39], s[90:91], 0, v[68:69]
	v_lshl_add_u64 v[40:41], v[38:39], 0, v[108:109]
	s_waitcnt vmcnt(5)
	ds_write2_b32 v2, v42, v43 offset1:1
	v_add_u32_e32 v2, 0x2948, v71
	ds_write2_b32 v2, v44, v45 offset1:1
	v_add_u32_e32 v2, 0x2d60, v71
	s_waitcnt vmcnt(4)
	ds_write2_b32 v2, v46, v47 offset1:1
	v_add_u32_e32 v2, 0x2d68, v71
	ds_write2_b32 v2, v48, v49 offset1:1
	v_add_u32_e32 v2, 0x3180, v71
	s_waitcnt vmcnt(3)
	ds_write2_b32 v2, v50, v51 offset1:1
	v_add_u32_e32 v2, 0x3188, v71
	ds_write2_b32 v2, v52, v53 offset1:1
	v_add_u32_e32 v2, 0x35a0, v71
	v_add_u32_e32 v42, 0x400, v119
	s_waitcnt vmcnt(2)
	ds_write2_b32 v2, v54, v55 offset1:1
	v_add_u32_e32 v2, 0x35a8, v71
	ds_write2_b32 v2, v56, v57 offset1:1
	v_add_u32_e32 v2, 0x39c0, v71
	s_waitcnt vmcnt(1)
	ds_write2_b32 v2, v58, v59 offset1:1
	v_add_u32_e32 v2, 0x39c8, v71
	ds_write2_b32 v2, v60, v61 offset1:1
	v_add_u32_e32 v2, 0x3de0, v71
	s_waitcnt vmcnt(0)
	ds_write2_b32 v2, v62, v63 offset1:1
	v_add_u32_e32 v2, 0x3de8, v71
	ds_write2_b32 v2, v64, v65 offset1:1
	s_waitcnt lgkmcnt(0)
	ds_read2_b32 v[6:7], v119 offset0:66 offset1:74
	ds_read2_b32 v[8:9], v119 offset0:99 offset1:107
	ds_read2_b32 v[10:11], v119 offset1:8
	ds_read2_b32 v[12:13], v119 offset0:33 offset1:41
	v_mov_b32_e32 v2, v67
	s_waitcnt lgkmcnt(3)
	v_mul_f32_e32 v3, 0x42000000, v6
	ds_read2_b32 v[14:15], v119 offset0:198 offset1:206
	ds_read2_b32 v[16:17], v119 offset0:231 offset1:239
	ds_read2_b32 v[18:19], v119 offset0:132 offset1:140
	ds_read2_b32 v[20:21], v119 offset0:165 offset1:173
	s_waitcnt lgkmcnt(5)
	v_mul_f32_e32 v5, 0x42000000, v10
	s_waitcnt lgkmcnt(4)
	v_mul_f32_e32 v6, 0x42000000, v12
	v_cvt_pk_fp8_f32 v2, v5, v6
	v_mul_f32_e32 v4, 0x42000000, v8
	s_waitcnt lgkmcnt(1)
	v_mul_f32_e32 v6, 0x42000000, v18
	s_waitcnt lgkmcnt(0)
	v_mul_f32_e32 v8, 0x42000000, v20
	v_cvt_pk_fp8_f32 v2, v3, v4 op_sel:[0,0,1]
	v_mov_b32_e32 v3, v67
	ds_read2_b32 v[22:23], v42 offset0:74 offset1:82
	ds_read2_b32 v[24:25], v42 offset0:107 offset1:115
	ds_read2_b32 v[26:27], v42 offset0:8 offset1:16
	ds_read2_b32 v[28:29], v42 offset0:41 offset1:49
	v_cvt_pk_fp8_f32 v3, v6, v8
	ds_read2_b32 v[30:31], v42 offset0:140 offset1:148
	ds_read2_b32 v[32:33], v42 offset0:173 offset1:181
	v_mul_f32_e32 v4, 0x42000000, v14
	v_mul_f32_e32 v5, 0x42000000, v16
	v_cvt_pk_fp8_f32 v3, v4, v5 op_sel:[0,0,1]
	s_waitcnt lgkmcnt(3)
	v_mul_f32_e32 v5, 0x42000000, v26
	s_waitcnt lgkmcnt(2)
	v_mul_f32_e32 v10, 0x42000000, v28
	v_mov_b32_e32 v4, v67
	ds_read2_b32 v[34:35], v42 offset0:206 offset1:214
	ds_read2_b32 v[36:37], v42 offset0:239 offset1:247
	v_cvt_pk_fp8_f32 v4, v5, v10
	s_waitcnt lgkmcnt(3)
	v_mul_f32_e32 v10, 0x42000000, v30
	s_waitcnt lgkmcnt(2)
	v_mul_f32_e32 v12, 0x42000000, v32
	v_mov_b32_e32 v5, v67
	v_cvt_pk_fp8_f32 v5, v10, v12
	v_mul_f32_e32 v6, 0x42000000, v22
	v_mul_f32_e32 v8, 0x42000000, v24
	v_cvt_pk_fp8_f32 v4, v6, v8 op_sel:[0,0,1]
	s_waitcnt lgkmcnt(1)
	v_mul_f32_e32 v6, 0x42000000, v34
	s_waitcnt lgkmcnt(0)
	v_mul_f32_e32 v8, 0x42000000, v36
	v_cvt_pk_fp8_f32 v5, v6, v8 op_sel:[0,0,1]
	v_mul_f32_e32 v6, 0x42000000, v13
	v_mul_f32_e32 v8, 0x42000000, v29
	global_store_dwordx4 v[40:41], v[2:5], off
	s_nop 1
	v_mul_f32_e32 v3, 0x42000000, v11
	v_mov_b32_e32 v2, v67
	v_mul_f32_e32 v4, 0x42000000, v7
	v_cvt_pk_fp8_f32 v2, v3, v6
	v_mul_f32_e32 v6, 0x42000000, v19
	v_mul_f32_e32 v7, 0x42000000, v21
	v_mov_b32_e32 v3, v67
	v_cvt_pk_fp8_f32 v3, v6, v7
	v_mul_f32_e32 v5, 0x42000000, v9
	v_cvt_pk_fp8_f32 v2, v4, v5 op_sel:[0,0,1]
	v_mul_f32_e32 v4, 0x42000000, v15
	v_mul_f32_e32 v5, 0x42000000, v17
	v_cvt_pk_fp8_f32 v3, v4, v5 op_sel:[0,0,1]
	v_mul_f32_e32 v5, 0x42000000, v27
	v_mov_b32_e32 v4, v67
	v_cvt_pk_fp8_f32 v4, v5, v8
	v_mul_f32_e32 v8, 0x42000000, v31
	v_mul_f32_e32 v9, 0x42000000, v33
	v_mov_b32_e32 v5, v67
	v_cvt_pk_fp8_f32 v5, v8, v9
	v_mul_f32_e32 v6, 0x42000000, v23
	v_mul_f32_e32 v7, 0x42000000, v25
	v_cvt_pk_fp8_f32 v4, v6, v7 op_sel:[0,0,1]
	v_mul_f32_e32 v6, 0x42000000, v35
	v_mul_f32_e32 v7, 0x42000000, v37
	ds_read2_b32 v[8:9], v119 offset0:82 offset1:90
	ds_read2_b32 v[10:11], v119 offset0:115 offset1:123
	ds_read2_b32 v[12:13], v119 offset0:16 offset1:24
	ds_read2_b32 v[14:15], v119 offset0:49 offset1:57
	v_cvt_pk_fp8_f32 v5, v6, v7 op_sel:[0,0,1]
	v_lshl_add_u64 v[6:7], v[38:39], 0, v[72:73]
	global_store_dwordx4 v[6:7], v[2:5], off
	s_waitcnt lgkmcnt(1)
	s_nop 0
	v_mul_f32_e32 v5, 0x42000000, v12
	s_waitcnt lgkmcnt(0)
	v_mul_f32_e32 v6, 0x42000000, v14
	v_mov_b32_e32 v2, v67
	v_cvt_pk_fp8_f32 v2, v5, v6
	ds_read2_b32 v[16:17], v119 offset0:214 offset1:222
	ds_read2_b32 v[18:19], v119 offset0:247 offset1:255
	ds_read2_b32 v[6:7], v119 offset0:148 offset1:156
	ds_read2_b32 v[20:21], v119 offset0:181 offset1:189
	v_mul_f32_e32 v3, 0x42000000, v8
	v_mul_f32_e32 v4, 0x42000000, v10
	v_cvt_pk_fp8_f32 v2, v3, v4 op_sel:[0,0,1]
	s_waitcnt lgkmcnt(1)
	v_mul_f32_e32 v6, 0x42000000, v6
	s_waitcnt lgkmcnt(0)
	v_mul_f32_e32 v8, 0x42000000, v20
	v_mov_b32_e32 v3, v67
	ds_read2_b32 v[22:23], v42 offset0:90 offset1:98
	ds_read2_b32 v[24:25], v42 offset0:123 offset1:131
	ds_read2_b32 v[26:27], v42 offset0:24 offset1:32
	ds_read2_b32 v[28:29], v42 offset0:57 offset1:65
	v_cvt_pk_fp8_f32 v3, v6, v8
	v_mul_f32_e32 v4, 0x42000000, v16
	v_mul_f32_e32 v5, 0x42000000, v18
	ds_read2_b32 v[30:31], v42 offset0:156 offset1:164
	ds_read2_b32 v[32:33], v42 offset0:189 offset1:197
	ds_read2_b32 v[34:35], v42 offset0:222 offset1:230
	v_cvt_pk_fp8_f32 v3, v4, v5 op_sel:[0,0,1]
	s_waitcnt lgkmcnt(4)
	v_mul_f32_e32 v5, 0x42000000, v26
	s_waitcnt lgkmcnt(3)
	v_mul_f32_e32 v10, 0x42000000, v28
	v_mov_b32_e32 v4, v67
	v_cvt_pk_fp8_f32 v4, v5, v10
	v_add_u32_e32 v5, 0x600, v119
	ds_read2_b32 v[36:37], v5 offset0:127 offset1:135
	s_waitcnt lgkmcnt(3)
	v_mul_f32_e32 v10, 0x42000000, v30
	s_waitcnt lgkmcnt(2)
	v_mul_f32_e32 v12, 0x42000000, v32
	v_mov_b32_e32 v5, v67
	v_cvt_pk_fp8_f32 v5, v10, v12
	v_mul_f32_e32 v6, 0x42000000, v22
	v_mul_f32_e32 v8, 0x42000000, v24
	v_cvt_pk_fp8_f32 v4, v6, v8 op_sel:[0,0,1]
	s_waitcnt lgkmcnt(1)
	v_mul_f32_e32 v6, 0x42000000, v34
	s_waitcnt lgkmcnt(0)
	v_mul_f32_e32 v8, 0x42000000, v36
	v_cvt_pk_fp8_f32 v5, v6, v8 op_sel:[0,0,1]
	v_mul_f32_e32 v8, 0x42000000, v9
	v_mul_f32_e32 v9, 0x42000000, v11
	v_mul_f32_e32 v10, 0x42000000, v13
	v_mul_f32_e32 v11, 0x42000000, v15
	v_mov_b32_e32 v6, v67
	v_cvt_pk_fp8_f32 v6, v10, v11
	v_mul_f32_e32 v10, 0x42000000, v7
	v_mul_f32_e32 v11, 0x42000000, v21
	v_mov_b32_e32 v7, v67
	v_cvt_pk_fp8_f32 v7, v10, v11
	v_cvt_pk_fp8_f32 v6, v8, v9 op_sel:[0,0,1]
	v_mul_f32_e32 v8, 0x42000000, v17
	v_mul_f32_e32 v9, 0x42000000, v19
	v_cvt_pk_fp8_f32 v7, v8, v9 op_sel:[0,0,1]
	v_mul_f32_e32 v9, 0x42000000, v27
	v_mul_f32_e32 v12, 0x42000000, v29
	v_mov_b32_e32 v8, v67
	v_cvt_pk_fp8_f32 v8, v9, v12
	v_mul_f32_e32 v12, 0x42000000, v31
	v_mul_f32_e32 v13, 0x42000000, v33
	v_mov_b32_e32 v9, v67
	v_cvt_pk_fp8_f32 v9, v12, v13
	v_mul_f32_e32 v10, 0x42000000, v23
	v_mul_f32_e32 v11, 0x42000000, v25
	v_cvt_pk_fp8_f32 v8, v10, v11 op_sel:[0,0,1]
	v_mul_f32_e32 v10, 0x42000000, v35
	v_mul_f32_e32 v11, 0x42000000, v37
	v_cvt_pk_fp8_f32 v9, v10, v11 op_sel:[0,0,1]
	v_lshl_add_u64 v[10:11], v[38:39], 0, v[78:79]
	global_store_dwordx4 v[10:11], v[2:5], off
	s_nop 1
	v_lshl_add_u64 v[2:3], v[38:39], 0, v[84:85]
	global_store_dwordx4 v[2:3], v[6:9], off
	s_waitcnt lgkmcnt(0)
.LBB0_31:
	s_andn2_b64 vcc, exec, s[24:25]
	s_cbranch_vccnz .LBB0_13
	s_cmp_lt_i32 s86, 44
	s_cselect_b64 s[24:25], -1, 0
	s_and_b64 s[90:91], s[24:25], exec
	s_cselect_b32 s86, s18, s22
	s_waitcnt lgkmcnt(0)
	s_add_u32 s2, s14, s88
	s_addc_u32 s17, s15, s87
	s_lshl_b32 s22, s19, 6
	s_mul_i32 s19, s19, 0x1b1000
	s_mul_hi_i32 s23, s22, 0x6c40
	s_add_u32 s2, s2, s19
	s_addc_u32 s17, s17, s23
	s_ashr_i32 s87, s86, 31
	s_lshl_b64 s[86:87], s[86:87], 2
	s_add_u32 s86, s2, s86
	s_addc_u32 s87, s17, s87
	s_and_b64 s[20:21], s[20:21], s[4:5]
	v_lshlrev_b32_e32 v66, 2, v118
	s_or_b64 s[20:21], s[24:25], s[20:21]
	v_lshl_add_u64 v[186:187], s[86:87], 0, v[66:67]
	v_mov_b32_e32 v2, 0
	v_mov_b32_e32 v6, 0
	v_mov_b32_e32 v7, 0
	v_mov_b32_e32 v8, 0
	v_mov_b32_e32 v9, 0
	s_and_saveexec_b64 s[24:25], s[20:21]
	s_cbranch_execz .LBB0_34
	v_lshl_add_u64 v[4:5], v[186:187], 0, v[122:123]
	global_load_dwordx4 v[6:9], v[4:5], off nt
.LBB0_34:
	s_or_b64 exec, exec, s[24:25]
	v_mov_b32_e32 v3, 0
	v_mov_b32_e32 v4, 0
	v_mov_b32_e32 v5, 0
	s_and_saveexec_b64 s[24:25], s[20:21]
	s_cbranch_execz .LBB0_36
	v_lshl_add_u64 v[2:3], v[186:187], 0, v[126:127]
	global_load_dwordx4 v[2:5], v[2:3], off nt
.LBB0_36:
	s_or_b64 exec, exec, s[24:25]
	v_mov_b32_e32 v10, 0
	v_mov_b32_e32 v14, 0
	v_mov_b32_e32 v15, 0
	v_mov_b32_e32 v16, 0
	v_mov_b32_e32 v17, 0
	s_and_saveexec_b64 s[24:25], s[20:21]
	s_cbranch_execz .LBB0_38
	v_lshl_add_u64 v[12:13], v[186:187], 0, v[130:131]
	global_load_dwordx4 v[14:17], v[12:13], off nt
.LBB0_38:
	s_or_b64 exec, exec, s[24:25]
	v_mov_b32_e32 v11, 0
	v_mov_b32_e32 v12, 0
	v_mov_b32_e32 v13, 0
	s_and_saveexec_b64 s[24:25], s[20:21]
	s_cbranch_execz .LBB0_40
	v_lshl_add_u64 v[10:11], v[186:187], 0, v[134:135]
	global_load_dwordx4 v[10:13], v[10:11], off nt
.LBB0_40:
	s_or_b64 exec, exec, s[24:25]
	v_mov_b32_e32 v18, 0
	v_mov_b32_e32 v22, 0
	v_mov_b32_e32 v23, 0
	v_mov_b32_e32 v24, 0
	v_mov_b32_e32 v25, 0
	s_and_saveexec_b64 s[24:25], s[20:21]
	s_cbranch_execz .LBB0_42
	v_lshl_add_u64 v[20:21], v[186:187], 0, v[138:139]
	global_load_dwordx4 v[22:25], v[20:21], off nt
.LBB0_42:
	s_or_b64 exec, exec, s[24:25]
	v_mov_b32_e32 v19, 0
	v_mov_b32_e32 v20, 0
	v_mov_b32_e32 v21, 0
	s_and_saveexec_b64 s[24:25], s[20:21]
	s_cbranch_execz .LBB0_44
	v_lshl_add_u64 v[18:19], v[186:187], 0, v[142:143]
	global_load_dwordx4 v[18:21], v[18:19], off nt
.LBB0_44:
	s_or_b64 exec, exec, s[24:25]
	v_mov_b32_e32 v26, 0
	v_mov_b32_e32 v30, 0
	v_mov_b32_e32 v31, 0
	v_mov_b32_e32 v32, 0
	v_mov_b32_e32 v33, 0
	s_and_saveexec_b64 s[24:25], s[20:21]
	s_cbranch_execz .LBB0_46
	v_lshl_add_u64 v[28:29], v[186:187], 0, v[146:147]
	global_load_dwordx4 v[30:33], v[28:29], off nt
.LBB0_46:
	s_or_b64 exec, exec, s[24:25]
	v_mov_b32_e32 v27, 0
	v_mov_b32_e32 v28, 0
	v_mov_b32_e32 v29, 0
	s_and_saveexec_b64 s[24:25], s[20:21]
	s_cbranch_execz .LBB0_48
	v_lshl_add_u64 v[26:27], v[186:187], 0, v[150:151]
	global_load_dwordx4 v[26:29], v[26:27], off nt
.LBB0_48:
	s_or_b64 exec, exec, s[24:25]
	v_mov_b32_e32 v34, 0
	v_mov_b32_e32 v38, 0
	v_mov_b32_e32 v39, 0
	v_mov_b32_e32 v40, 0
	v_mov_b32_e32 v41, 0
	s_and_saveexec_b64 s[24:25], s[20:21]
	s_cbranch_execz .LBB0_50
	v_lshl_add_u64 v[36:37], v[186:187], 0, v[154:155]
	global_load_dwordx4 v[38:41], v[36:37], off nt
.LBB0_50:
	s_or_b64 exec, exec, s[24:25]
	v_mov_b32_e32 v35, 0
	v_mov_b32_e32 v36, 0
	v_mov_b32_e32 v37, 0
	s_and_saveexec_b64 s[24:25], s[20:21]
	s_cbranch_execz .LBB0_52
	v_lshl_add_u64 v[34:35], v[186:187], 0, v[158:159]
	global_load_dwordx4 v[34:37], v[34:35], off nt
.LBB0_52:
	s_or_b64 exec, exec, s[24:25]
	v_mov_b32_e32 v42, 0
	v_mov_b32_e32 v46, 0
	v_mov_b32_e32 v47, 0
	v_mov_b32_e32 v48, 0
	v_mov_b32_e32 v49, 0
	s_and_saveexec_b64 s[24:25], s[20:21]
	s_cbranch_execz .LBB0_54
	v_lshl_add_u64 v[44:45], v[186:187], 0, v[162:163]
	global_load_dwordx4 v[46:49], v[44:45], off nt
.LBB0_54:
	s_or_b64 exec, exec, s[24:25]
	v_mov_b32_e32 v43, 0
	v_mov_b32_e32 v44, 0
	v_mov_b32_e32 v45, 0
	s_and_saveexec_b64 s[24:25], s[20:21]
	s_cbranch_execz .LBB0_56
	v_lshl_add_u64 v[42:43], v[186:187], 0, v[166:167]
	global_load_dwordx4 v[42:45], v[42:43], off nt
.LBB0_56:
	s_or_b64 exec, exec, s[24:25]
	v_mov_b32_e32 v50, 0
	v_mov_b32_e32 v54, 0
	v_mov_b32_e32 v55, 0
	v_mov_b32_e32 v56, 0
	v_mov_b32_e32 v57, 0
	s_and_saveexec_b64 s[24:25], s[20:21]
	s_cbranch_execz .LBB0_58
	v_lshl_add_u64 v[52:53], v[186:187], 0, v[170:171]
	global_load_dwordx4 v[54:57], v[52:53], off nt
.LBB0_58:
	s_or_b64 exec, exec, s[24:25]
	v_mov_b32_e32 v51, 0
	v_mov_b32_e32 v52, 0
	v_mov_b32_e32 v53, 0
	s_and_saveexec_b64 s[24:25], s[20:21]
	s_cbranch_execz .LBB0_60
	v_lshl_add_u64 v[50:51], v[186:187], 0, v[174:175]
	global_load_dwordx4 v[50:53], v[50:51], off nt
.LBB0_60:
	s_or_b64 exec, exec, s[24:25]
	v_mov_b32_e32 v58, 0
	v_mov_b32_e32 v62, 0
	v_mov_b32_e32 v63, 0
	v_mov_b32_e32 v64, 0
	v_mov_b32_e32 v65, 0
	s_and_saveexec_b64 s[24:25], s[20:21]
	s_cbranch_execz .LBB0_62
	v_lshl_add_u64 v[60:61], v[186:187], 0, v[178:179]
	global_load_dwordx4 v[62:65], v[60:61], off nt
.LBB0_62:
	s_or_b64 exec, exec, s[24:25]
	s_ashr_i32 s23, s22, 31
	v_mov_b32_e32 v59, 0
	v_mov_b32_e32 v60, 0
	v_mov_b32_e32 v61, 0
	s_and_saveexec_b64 s[24:25], s[20:21]
	s_cbranch_execz .LBB0_12
	v_lshl_add_u64 v[58:59], v[186:187], 0, v[182:183]
	global_load_dwordx4 v[58:61], v[58:59], off nt
	s_branch .LBB0_12

.LBB0_149:
	s_mov_b32 s25, s2
	s_add_i32 s2, s2, 2
	s_mul_hi_i32 s6, s2, 0x78787879
	s_lshr_b32 s7, s6, 31
	s_ashr_i32 s6, s6, 11
	s_add_i32 s6, s6, s7
	s_mul_i32 s7, s6, 0xffffef00
	s_add_i32 s28, s25, s7
	s_add_i32 s29, s28, 2
	s_cmpk_lt_i32 s29, 0x100
	s_cselect_b64 s[14:15], -1, 0
	s_and_b64 s[26:27], s[14:15], exec
	s_cselect_b32 s13, 16, s6
	s_ashr_i32 s7, s6, 31
	s_addk_i32 s28, 0xff02
	s_ashr_i32 s26, s29, 31
	s_and_b64 s[14:15], s[14:15], exec
	v_readlane_b32 s36, v252, 12
	v_readlane_b32 s40, v252, 14
	s_cselect_b32 s14, s29, s28
	v_readlane_b32 s37, v252, 13
	v_readlane_b32 s41, v252, 15
	s_cselect_b32 s28, 20, 24
	s_cselect_b32 s15, s26, 0
	s_cselect_b32 s26, s41, s37
	s_cselect_b32 s27, s40, s36
	s_lshl_b64 s[6:7], s[6:7], s28
	s_add_u32 s27, s27, s6
	s_addc_u32 s26, s26, s7
	s_lshl_b64 s[6:7], s[14:15], 12
	s_add_u32 s6, s27, s6
	s_addc_u32 s7, s26, s7
	v_lshlrev_b64 v[8:9], 2, v[60:61]
	v_lshl_add_u64 v[10:11], s[6:7], 0, v[8:9]
	s_add_i32 s6, s25, 3
	s_mul_hi_i32 s6, s6, 0x78787879
	s_lshr_b32 s7, s6, 31
	s_ashr_i32 s6, s6, 11
	s_add_i32 s6, s6, s7
	s_mul_i32 s7, s6, 0xffffef00
	s_add_i32 s14, s25, s7
	s_add_i32 s25, s14, 3
	s_cmpk_lt_i32 s25, 0x100
	s_cselect_b64 s[38:39], -1, 0
	s_ashr_i32 s7, s6, 31
	s_ashr_i32 s26, s25, 31
	s_add_i32 s27, s14, 0xffffff03
	s_and_b64 s[14:15], s[38:39], exec
	s_cselect_b32 s15, s26, 0
	s_cselect_b32 s26, 20, 24
	s_cselect_b32 s14, s25, s27
	s_cselect_b32 s25, s41, s37
	s_cselect_b32 s28, s40, s36
	s_lshl_b64 s[26:27], s[6:7], s26
	s_add_u32 s7, s28, s26
	s_addc_u32 s25, s25, s27
	s_lshl_b64 s[14:15], s[14:15], 12
	s_add_u32 s14, s7, s14
	s_addc_u32 s15, s25, s15
	v_lshl_add_u64 v[12:13], s[14:15], 0, v[8:9]
	global_load_dwordx4 v[40:43], v[10:11], off offset:16 nt
	global_load_dwordx4 v[44:47], v[10:11], off nt
	global_load_dwordx4 v[32:35], v[10:11], off offset:2064 nt
	global_load_dwordx4 v[36:39], v[10:11], off offset:2048 nt
	global_load_dwordx4 v[16:19], v[12:13], off offset:16 nt
	global_load_dwordx4 v[20:23], v[12:13], off nt
	s_nop 0
	global_load_dwordx4 v[8:11], v[12:13], off offset:2064 nt
	s_nop 0
	global_load_dwordx4 v[12:15], v[12:13], off offset:2048 nt
	s_cmp_eq_u32 s13, s4
	s_cbranch_scc1 .LBB0_151
	s_mul_i32 s7, s13, 0x6000
	s_mul_hi_i32 s4, s13, 0x6000
	s_add_u32 s14, s60, s7
	global_load_dwordx4 v[24:27], v[48:49], off offset:16
	global_load_dwordx4 v[28:31], v[48:49], off
	s_addc_u32 s15, s63, s4
	v_lshl_add_u64 v[84:85], v[60:61], 2, s[14:15]
	v_add_co_u32_e32 v0, vcc, 0x1000, v84
	v_lshl_add_u64 v[58:59], v[84:85], 0, s[84:85]
	s_nop 0
	v_addc_co_u32_e32 v1, vcc, 0, v85, vcc
	global_load_dwordx4 v[54:57], v[0:1], off
	global_load_dwordx4 v[62:65], v[58:59], off offset:16
	global_load_dwordx4 v[4:7], v[84:85], off offset:16
	s_nop 0
	global_load_dwordx4 v[0:3], v[84:85], off
	global_load_dwordx4 v[72:75], v[48:49], off offset:2048
	global_load_dwordx4 v[66:69], v[48:49], off offset:2064
	global_load_dwordx4 v[76:79], v[58:59], off offset:2064
	global_load_dwordx4 v[80:83], v[58:59], off offset:2048
	s_mov_b32 s4, s13
	s_waitcnt vmcnt(0)
	v_pk_add_f32 v[56:57], v[56:57], 1.0 op_sel_hi:[1,0]
	v_pk_add_f32 v[54:55], v[54:55], 1.0 op_sel_hi:[1,0]
	s_waitcnt vmcnt(6)
	v_pk_add_f32 v[58:59], v[64:65], 1.0 op_sel_hi:[1,0]
	v_pk_add_f32 v[62:63], v[62:63], 1.0 op_sel_hi:[1,0]
	v_pk_mul_f32 v[56:57], v[30:31], v[56:57]
	v_pk_mul_f32 v[58:59], v[26:27], v[58:59]
	v_pk_mul_f32 v[54:55], v[28:29], v[54:55]
	v_pk_mul_f32 v[62:63], v[24:25], v[62:63]
	global_load_dwordx4 v[24:27], v[84:85], off offset:2064
	global_load_dwordx4 v[28:31], v[84:85], off offset:2048
	s_waitcnt vmcnt(2)
	v_pk_add_f32 v[64:65], v[82:83], 1.0 op_sel_hi:[1,0]
	v_pk_add_f32 v[70:71], v[78:79], 1.0 op_sel_hi:[1,0]
	v_pk_add_f32 v[78:79], v[80:81], 1.0 op_sel_hi:[1,0]
	v_pk_add_f32 v[76:77], v[76:77], 1.0 op_sel_hi:[1,0]
	v_pk_mul_f32 v[68:69], v[68:69], v[70:71]
	v_pk_mul_f32 v[64:65], v[74:75], v[64:65]
	v_pk_mul_f32 v[70:71], v[66:67], v[76:77]
	v_pk_mul_f32 v[66:67], v[72:73], v[78:79]
